# conversion stream loops: counted vmcnt waits so next item loads stay in flight (double buffering) instead of vmcnt(0) drains
# baseline (speedup 1.0000x reference)
; __device__ __forceinline__ void t128_load(const float* W, int N, int item, int lane, f32x4 (&v)[16]) {
;     const int nblk = N / 32, kb = item / nblk, nb = item % nblk, k0 = 128 * kb, n0 = 32 * nb;
; #pragma unroll
;     for (int i = 0; i < 16; ++i) v[i] = __builtin_nontemporal_load((const f32x4*)(W + (size_t)(k0 + i * 8 + (lane >> 3)) * N + n0 + (lane & 7) * 4));
; }
; __device__ __forceinline__ void cs_load(int it, int lane, const float* w_gu, const float* w_d, f32x4 (&v)[16]) {
;     if (it < I_D) { constexpr int per = (DFF / 128) * (D / 32); t128_load(w_d + (size_t)(it / per) * DFF * D, D, it % per, lane, v); }
;     else { const int r = it - I_D; constexpr int per = (D / 128) * (4096 / 32); t128_load(w_gu + (size_t)(r / per) * D * 4096, 4096, r % per, lane, v); }
; }
; __device__ __forceinline__ void cs_store(const Ctx& c, int it, const f32x4 (&v)[16], unsigned char* Wgu, unsigned char* Wd) {
;     if (it < I_D) { constexpr int per = (DFF / 128) * (D / 32); t128_store<0>(c, v, DFF, D, Wd + (size_t)(it / per) * D * DFF, it % per); }
;     else { const int r = it - I_D; constexpr int per = (D / 128) * (4096 / 32); t128_store<1>(c, v, D, 4096, Wgu + (size_t)(r / per) * 4096 * D, r % per); }
; }
; __device__ __forceinline__ int conv_stream(const Ctx& c, int j, int first, int step, const unsigned* stop, const float* w_gu, const float* w_d, unsigned char* Wgu, unsigned char* Wd) {
;     int i = first;
;     if (j + CONV_SLOTS * i >= CONV_TOTAL) return i;
;     if (stop && stop_poll(c, stop) >= STOP_AT) return i;
;     f32x4 va[16], vb[16];
;     cs_load(j + CONV_SLOTS * i, c.lane, w_gu, w_d, va);
.LBB0_257:
	v_lshlrev_b32_e32 v2, 2, v1
	v_and_b32_e32 v130, 28, v2
	v_mov_b32_e32 v133, 0
	v_lshlrev_b32_e32 v132, 2, v130
	v_ashrrev_i32_e32 v59, 31, v58
	v_lshl_add_u64 v[60:61], s[44:45], 0, v[132:133]
	v_lshlrev_b64 v[2:3], s38, v[58:59]
	v_lshl_add_u64 v[10:11], v[60:61], 0, v[2:3]
	v_add_u32_e32 v2, 8, v58
	v_ashrrev_i32_e32 v3, 31, v2
	v_lshlrev_b64 v[2:3], s38, v[2:3]
	v_lshl_add_u64 v[12:13], v[60:61], 0, v[2:3]
	global_load_dwordx4 v[6:9], v[10:11], off nt
	global_load_dwordx4 v[2:5], v[12:13], off nt
	v_add_u32_e32 v10, 16, v58
	v_ashrrev_i32_e32 v11, 31, v10
	v_lshlrev_b64 v[10:11], s38, v[10:11]
	v_lshl_add_u64 v[18:19], v[60:61], 0, v[10:11]
	v_add_u32_e32 v10, 24, v58
	v_ashrrev_i32_e32 v11, 31, v10
	v_lshlrev_b64 v[10:11], s38, v[10:11]
	v_lshl_add_u64 v[20:21], v[60:61], 0, v[10:11]
	global_load_dwordx4 v[14:17], v[18:19], off nt
	global_load_dwordx4 v[10:13], v[20:21], off nt
	v_add_u32_e32 v18, 32, v58
	v_ashrrev_i32_e32 v19, 31, v18
	v_lshlrev_b64 v[18:19], s38, v[18:19]
	v_lshl_add_u64 v[26:27], v[60:61], 0, v[18:19]
	v_add_u32_e32 v18, 40, v58
	v_ashrrev_i32_e32 v19, 31, v18
	v_lshlrev_b64 v[18:19], s38, v[18:19]
	v_lshl_add_u64 v[28:29], v[60:61], 0, v[18:19]
	global_load_dwordx4 v[22:25], v[26:27], off nt
	global_load_dwordx4 v[18:21], v[28:29], off nt
	v_add_u32_e32 v26, 48, v58
	v_ashrrev_i32_e32 v27, 31, v26
	v_lshlrev_b64 v[26:27], s38, v[26:27]
	v_lshl_add_u64 v[34:35], v[60:61], 0, v[26:27]
	v_add_u32_e32 v26, 56, v58
	v_ashrrev_i32_e32 v27, 31, v26
	v_lshlrev_b64 v[26:27], s38, v[26:27]
	v_lshl_add_u64 v[36:37], v[60:61], 0, v[26:27]
	global_load_dwordx4 v[30:33], v[34:35], off nt
	global_load_dwordx4 v[26:29], v[36:37], off nt
	v_add_u32_e32 v34, 64, v58
	v_ashrrev_i32_e32 v35, 31, v34
	v_lshlrev_b64 v[34:35], s38, v[34:35]
	v_lshl_add_u64 v[42:43], v[60:61], 0, v[34:35]
	v_add_u32_e32 v34, 0x48, v58
	v_ashrrev_i32_e32 v35, 31, v34
	v_lshlrev_b64 v[34:35], s38, v[34:35]
	v_lshl_add_u64 v[44:45], v[60:61], 0, v[34:35]
	global_load_dwordx4 v[38:41], v[42:43], off nt
	global_load_dwordx4 v[34:37], v[44:45], off nt
	v_add_u32_e32 v42, 0x50, v58
	v_ashrrev_i32_e32 v43, 31, v42
	v_lshlrev_b64 v[42:43], s38, v[42:43]
	v_lshl_add_u64 v[50:51], v[60:61], 0, v[42:43]
	v_add_u32_e32 v42, 0x58, v58
	v_ashrrev_i32_e32 v43, 31, v42
	v_lshlrev_b64 v[42:43], s38, v[42:43]
	v_lshl_add_u64 v[52:53], v[60:61], 0, v[42:43]
	global_load_dwordx4 v[46:49], v[50:51], off nt
	global_load_dwordx4 v[42:45], v[52:53], off nt
	v_add_u32_e32 v50, 0x60, v58
	v_ashrrev_i32_e32 v51, 31, v50
	v_lshlrev_b64 v[50:51], s38, v[50:51]
	v_lshl_add_u64 v[62:63], v[60:61], 0, v[50:51]
	v_add_u32_e32 v50, 0x68, v58
	v_ashrrev_i32_e32 v51, 31, v50
	v_lshlrev_b64 v[50:51], s38, v[50:51]
	v_lshl_add_u64 v[64:65], v[60:61], 0, v[50:51]
	global_load_dwordx4 v[54:57], v[62:63], off nt
	global_load_dwordx4 v[50:53], v[64:65], off nt
	v_add_u32_e32 v62, 0x70, v58
	v_ashrrev_i32_e32 v63, 31, v62
	v_add_u32_e32 v58, 0x78, v58
	v_lshlrev_b64 v[62:63], s38, v[62:63]
	v_ashrrev_i32_e32 v59, 31, v58
	v_lshl_add_u64 v[68:69], v[60:61], 0, v[62:63]
	v_lshlrev_b64 v[58:59], s38, v[58:59]
	v_lshl_add_u64 v[70:71], v[60:61], 0, v[58:59]
	global_load_dwordx4 v[62:65], v[68:69], off nt
	global_load_dwordx4 v[58:61], v[70:71], off nt
	s_add_u32 s38, s30, 0x1e00000
	s_addc_u32 s39, s31, 0
	s_add_u32 s9, s30, 0x21e00000
	v_lshlrev_b32_e32 v67, 4, v1
	s_addc_u32 s14, s31, 0
	s_lshl_b64 s[20:21], s[42:43], 2
	v_and_b32_e32 v134, 0x70, v67
	v_mov_b32_e32 v67, v133
	s_add_u32 s15, s4, s20
	s_mul_i32 s20, s18, 0x4200
	v_lshl_add_u64 v[66:67], s[38:39], 0, v[66:67]
	v_mov_b32_e32 v135, v133
	s_addc_u32 s16, s5, s21
	s_add_i32 s20, s20, 0
	v_mul_u32_u24_e32 v72, 0x84, v134
	v_lshl_add_u64 v[136:137], v[66:67], 0, v[134:135]
	v_lshlrev_b32_e32 v66, 2, v131
	v_add_u32_e32 v68, s20, v132
	s_movk_i32 s21, 0x84
	v_add3_u32 v150, s20, v72, v66
	s_lshl_b32 s20, s8, 6
	v_mad_i32_i24 v146, v131, s21, v68
	s_and_b32 s20, s20, 0xf00
	s_lshr_b32 s21, s17, 4
	s_and_b32 s17, s17, 0x60
	s_and_b32 s21, s21, 0x80
	s_or_b32 s17, s17, s20
	v_or_b32_e32 v147, 8, v131
	v_or_b32_e32 v148, 16, v131
	v_or_b32_e32 v149, 24, v131
	s_or_b32 s17, s17, s21
	v_add_lshl_u32 v138, s17, v131, 11
	v_add_lshl_u32 v140, s17, v147, 11
	v_add_lshl_u32 v142, s17, v148, 11
	v_add_lshl_u32 v144, s17, v149, 11
	s_lshl_b32 s17, s2, 3
	s_andn2_b32 s17, s17, 63
	s_add_i32 s17, s18, s17
	s_lshl_b32 s18, s19, 3
	v_mul_i32_i24_e32 v69, 0x84, v147
	v_mul_i32_i24_e32 v70, 0x84, v148
	v_mul_i32_i24_e32 v71, 0x84, v149
	s_add_i32 s17, s17, s18
	s_mov_b32 s43, 0
	v_cmp_eq_u32_e64 s[4:5], 0, v1
	v_mov_b32_e32 v139, v133
	v_mov_b32_e32 v141, v133
	v_mov_b32_e32 v143, v133
	v_mov_b32_e32 v145, v133
	s_add_i32 s19, s17, 0x400
	s_add_i32 s18, 0, 0x23e00
	v_add_u32_e32 v151, v68, v69
	v_add_u32_e32 v152, v68, v70
	v_add_u32_e32 v153, v68, v71
	s_mov_b32 s17, 0
	s_waitcnt vmcnt(0)
	s_branch .LBB0_259

; #define LAS __attribute__((address_space(3)))
; __device__ __forceinline__ unsigned stop_poll(const Ctx& c, const unsigned* p) {
;     volatile LAS unsigned* w = (volatile LAS unsigned*)(c.lds + STOPW_OFF);
;     if (c.wave == 0) { const unsigned v = __hip_atomic_load(p, __ATOMIC_RELAXED, __HIP_MEMORY_SCOPE_AGENT); if (c.lane == 0) *w = v; return (unsigned)__builtin_amdgcn_readfirstlane((int)v); }
;     return *w;
; __device__ __forceinline__ int conv_stream(const Ctx& c, int j, int first, int step, const unsigned* stop, const float* w_gu, const float* w_d, unsigned char* Wgu, unsigned char* Wd) {
;     ...
;         { const int i2 = i + step; const bool more = j + CONV_SLOTS * i2 < CONV_TOTAL && !(stop && stop_poll(c, stop) >= STOP_AT);
;           cs_load(j + CONV_SLOTS * (more ? i2 : i), c.lane, w_gu, w_d, vb);
;           cs_store(c, j + CONV_SLOTS * i, va, Wgu, Wd); i = i2; if (!more) break; }
;         { const int i2 = i + step; const bool more = j + CONV_SLOTS * i2 < CONV_TOTAL && !(stop && stop_poll(c, stop) >= STOP_AT);
.LBB0_259:
	s_add_i32 s24, s19, 0xfffffc00
	s_cmp_gt_i32 s24, 0x17fff
	s_mov_b64 s[44:45], 0
	s_cbranch_scc1 .LBB0_267
	s_mov_b64 s[44:45], -1
	s_and_b64 vcc, exec, s[6:7]
	s_cbranch_vccz .LBB0_262
	s_waitcnt vmcnt(4)
	v_mov_b32_e32 v66, s18
	ds_read_b32 v66, v66
	s_mov_b64 s[44:45], 0
	s_waitcnt lgkmcnt(0)
	v_readfirstlane_b32 s20, v66

; __device__ __forceinline__ void t128_load(const float* W, int N, int item, int lane, f32x4 (&v)[16]) {
;     const int nblk = N / 32, kb = item / nblk, nb = item % nblk, k0 = 128 * kb, n0 = 32 * nb;
; #pragma unroll
;     for (int i = 0; i < 16; ++i) v[i] = __builtin_nontemporal_load((const f32x4*)(W + (size_t)(k0 + i * 8 + (lane >> 3)) * N + n0 + (lane & 7) * 4));
; }
; __device__ __forceinline__ void cs_load(int it, int lane, const float* w_gu, const float* w_d, f32x4 (&v)[16]) {
;     if (it < I_D) { constexpr int per = (DFF / 128) * (D / 32); t128_load(w_d + (size_t)(it / per) * DFF * D, D, it % per, lane, v); }
;     else { const int r = it - I_D; constexpr int per = (D / 128) * (4096 / 32); t128_load(w_gu + (size_t)(r / per) * D * 4096, 4096, r % per, lane, v); }
.LBB0_271:
	s_waitcnt vmcnt(4)
	v_or_b32_e32 v122, s21, v131
	v_ashrrev_i32_e32 v123, 31, v122
	v_lshlrev_b64 v[66:67], s46, v[122:123]
	v_add_u32_e32 v68, 8, v122
	v_add_u32_e32 v74, 16, v122
	v_add_u32_e32 v76, 24, v122
	v_add_u32_e32 v82, 32, v122
	v_add_u32_e32 v84, 40, v122
	v_add_u32_e32 v90, 48, v122
	v_add_u32_e32 v92, 56, v122
	v_add_u32_e32 v98, 64, v122
	v_add_u32_e32 v100, 0x48, v122
	v_add_u32_e32 v106, 0x50, v122
	v_add_u32_e32 v108, 0x58, v122
	v_add_u32_e32 v114, 0x60, v122
	v_add_u32_e32 v116, 0x68, v122
	v_add_u32_e32 v126, 0x70, v122
	v_add_u32_e32 v122, 0x78, v122
	v_lshlrev_b32_e32 v132, 2, v130
	v_ashrrev_i32_e32 v69, 31, v68
	v_ashrrev_i32_e32 v75, 31, v74
	v_ashrrev_i32_e32 v77, 31, v76
	v_ashrrev_i32_e32 v83, 31, v82
	v_ashrrev_i32_e32 v85, 31, v84
	v_ashrrev_i32_e32 v91, 31, v90
	v_ashrrev_i32_e32 v93, 31, v92
	v_ashrrev_i32_e32 v99, 31, v98
	v_ashrrev_i32_e32 v101, 31, v100
	v_ashrrev_i32_e32 v107, 31, v106
	v_ashrrev_i32_e32 v109, 31, v108
	v_ashrrev_i32_e32 v115, 31, v114
	v_ashrrev_i32_e32 v117, 31, v116
	v_ashrrev_i32_e32 v127, 31, v126
	v_ashrrev_i32_e32 v123, 31, v122
	v_lshl_add_u64 v[124:125], s[48:49], 0, v[132:133]
	v_lshlrev_b64 v[68:69], s46, v[68:69]
	v_lshlrev_b64 v[74:75], s46, v[74:75]
	v_lshlrev_b64 v[76:77], s46, v[76:77]
	v_lshlrev_b64 v[82:83], s46, v[82:83]
	v_lshlrev_b64 v[84:85], s46, v[84:85]
	v_lshlrev_b64 v[90:91], s46, v[90:91]
	v_lshlrev_b64 v[92:93], s46, v[92:93]
	v_lshlrev_b64 v[98:99], s46, v[98:99]
	v_lshlrev_b64 v[100:101], s46, v[100:101]
	v_lshlrev_b64 v[106:107], s46, v[106:107]
	v_lshlrev_b64 v[108:109], s46, v[108:109]
	v_lshlrev_b64 v[114:115], s46, v[114:115]
	v_lshlrev_b64 v[116:117], s46, v[116:117]
	v_lshlrev_b64 v[126:127], s46, v[126:127]
	v_lshlrev_b64 v[122:123], s46, v[122:123]
	v_lshl_add_u64 v[66:67], v[124:125], 0, v[66:67]
	v_lshl_add_u64 v[68:69], v[124:125], 0, v[68:69]
	v_lshl_add_u64 v[74:75], v[124:125], 0, v[74:75]
	v_lshl_add_u64 v[76:77], v[124:125], 0, v[76:77]
	v_lshl_add_u64 v[82:83], v[124:125], 0, v[82:83]
	v_lshl_add_u64 v[84:85], v[124:125], 0, v[84:85]
	v_lshl_add_u64 v[90:91], v[124:125], 0, v[90:91]
	v_lshl_add_u64 v[92:93], v[124:125], 0, v[92:93]
	v_lshl_add_u64 v[98:99], v[124:125], 0, v[98:99]
	v_lshl_add_u64 v[100:101], v[124:125], 0, v[100:101]
	v_lshl_add_u64 v[106:107], v[124:125], 0, v[106:107]
	v_lshl_add_u64 v[108:109], v[124:125], 0, v[108:109]
	v_lshl_add_u64 v[114:115], v[124:125], 0, v[114:115]
	v_lshl_add_u64 v[116:117], v[124:125], 0, v[116:117]
	v_lshl_add_u64 v[126:127], v[124:125], 0, v[126:127]
	v_lshl_add_u64 v[122:123], v[124:125], 0, v[122:123]
	global_load_dwordx4 v[70:73], v[66:67], off nt
	s_nop 0
	global_load_dwordx4 v[66:69], v[68:69], off nt
	s_nop 0
	global_load_dwordx4 v[78:81], v[74:75], off nt
	s_nop 0
	global_load_dwordx4 v[74:77], v[76:77], off nt
	s_nop 0
	global_load_dwordx4 v[86:89], v[82:83], off nt
	s_nop 0
	global_load_dwordx4 v[82:85], v[84:85], off nt
	s_nop 0
	global_load_dwordx4 v[94:97], v[90:91], off nt
	s_nop 0
	global_load_dwordx4 v[90:93], v[92:93], off nt
	s_nop 0
	global_load_dwordx4 v[102:105], v[98:99], off nt
	s_nop 0
	global_load_dwordx4 v[98:101], v[100:101], off nt
	s_nop 0
	global_load_dwordx4 v[110:113], v[106:107], off nt
	s_nop 0
	global_load_dwordx4 v[106:109], v[108:109], off nt
	s_nop 0
	global_load_dwordx4 v[118:121], v[114:115], off nt
	s_nop 0
	global_load_dwordx4 v[114:117], v[116:117], off nt
	s_nop 0
	global_load_dwordx4 v[126:129], v[126:127], off nt
	s_nop 0
	global_load_dwordx4 v[122:125], v[122:123], off nt
	s_add_i32 s26, s19, 0xfffff800
	s_mov_b64 s[46:47], -1
	s_cmpk_gt_i32 s26, 0x7fff
	v_add_u32_e32 v156, 0x1080, v146
	v_add_u32_e32 v157, 0x1088, v146
	v_add_u32_e32 v158, 0x14a0, v146
	v_add_u32_e32 v159, 0x14a8, v146
	v_add_u32_e32 v160, 0x18c0, v146
	v_add_u32_e32 v161, 0x18c8, v146
	v_add_u32_e32 v162, 0x1ce0, v146
	v_add_u32_e32 v163, 0x1ce8, v146
	v_add_u32_e32 v164, 0x2100, v146
	v_add_u32_e32 v165, 0x2108, v146
	v_add_u32_e32 v166, 0x2520, v146
	v_add_u32_e32 v167, 0x2528, v146
	v_add_u32_e32 v168, 0x2940, v146
	v_add_u32_e32 v169, 0x2948, v146
	v_add_u32_e32 v170, 0x2d60, v146
	v_add_u32_e32 v171, 0x2d68, v146
	v_add_u32_e32 v172, 0x3180, v146
	v_add_u32_e32 v173, 0x3188, v146
	v_add_u32_e32 v174, 0x35a0, v146
	v_add_u32_e32 v175, 0x35a8, v146
	v_add_u32_e32 v176, 0x39c0, v146
	v_add_u32_e32 v177, 0x39c8, v146
	v_add_u32_e32 v178, 0x3de0, v146
	v_add_u32_e32 v179, 0x3de8, v146
	v_add_u32_e32 v155, 0x400, v150
	v_add_u32_e32 v154, 0x600, v150
	s_cbranch_scc0 .LBB0_290
; #define LAS __attribute__((address_space(3)))
; #define LDS_WAIT() asm volatile("s_waitcnt lgkmcnt(0)" ::: "memory")
; template <int MODE>
; __device__ __forceinline__ void t128_store(const Ctx& c, const f32x4 (&v)[16], int K, int N, unsigned char* WT, int item) {
;     LAS float* scr = (LAS float*)(c.lds + c.wave * CONV_SCR);
;     const int nblk = N / 32, kb = item / nblk, nb = item % nblk, k0 = 128 * kb, n0 = 32 * nb, lane = c.lane;
; #pragma unroll
;     for (int i = 0; i < 16; ++i) { LAS float* d = scr + (i * 8 + (lane >> 3)) * 33 + (lane & 7) * 4; d[0] = v[i].x; d[1] = v[i].y; d[2] = v[i].z; d[3] = v[i].w; }
;     LDS_WAIT(); asm volatile("" ::: "memory");
;     const int cc = lane & 7;
; #pragma unroll
;     for (int j = 0; j < 4; ++j) { const int n = (lane >> 3) + 8 * j; const LAS float* s = scr + (16 * cc) * 33 + n; int w[4];
; #pragma unroll
;         for (int q = 0; q < 4; ++q) { int t = 0; t = __builtin_amdgcn_cvt_pk_fp8_f32(s[(4 * q) * 33] * WSCALE, s[(4 * q + 1) * 33] * WSCALE, t, false);
;             t = __builtin_amdgcn_cvt_pk_fp8_f32(s[(4 * q + 2) * 33] * WSCALE, s[(4 * q + 3) * 33] * WSCALE, t, true); w[q] = t; }
;         const int dr = drow_of<MODE>(n0 + n);
;         __builtin_nontemporal_store((u32x4){(unsigned)w[0], (unsigned)w[1], (unsigned)w[2], (unsigned)w[3]}, (u32x4*)(WT + (size_t)dr * K + k0 + 16 * cc)); }
;     LDS_WAIT(); asm volatile("" ::: "memory");
; }
	s_nop 0
	ds_write2_b32 v146, v6, v7 offset1:1
	ds_write2_b32 v146, v8, v9 offset0:2 offset1:3
	ds_write2_b32 v151, v2, v3 offset1:1
	ds_write2_b32 v151, v4, v5 offset0:2 offset1:3
	ds_write2_b32 v152, v14, v15 offset1:1
	ds_write2_b32 v152, v16, v17 offset0:2 offset1:3
	ds_write2_b32 v153, v10, v11 offset1:1
	ds_write2_b32 v153, v12, v13 offset0:2 offset1:3
	ds_write2_b32 v156, v22, v23 offset1:1
	ds_write2_b32 v157, v24, v25 offset1:1
	ds_write2_b32 v158, v18, v19 offset1:1
	ds_write2_b32 v159, v20, v21 offset1:1
	ds_write2_b32 v160, v30, v31 offset1:1
	ds_write2_b32 v161, v32, v33 offset1:1
	ds_write2_b32 v162, v26, v27 offset1:1
	ds_write2_b32 v163, v28, v29 offset1:1
	ds_write2_b32 v164, v38, v39 offset1:1
	ds_write2_b32 v165, v40, v41 offset1:1
	ds_write2_b32 v166, v34, v35 offset1:1
	ds_write2_b32 v167, v36, v37 offset1:1
	ds_write2_b32 v168, v46, v47 offset1:1
	ds_write2_b32 v169, v48, v49 offset1:1
	ds_write2_b32 v170, v42, v43 offset1:1
	ds_write2_b32 v171, v44, v45 offset1:1
	ds_write2_b32 v172, v54, v55 offset1:1
	ds_write2_b32 v173, v56, v57 offset1:1
	ds_write2_b32 v174, v50, v51 offset1:1
	ds_write2_b32 v175, v52, v53 offset1:1
	ds_write2_b32 v176, v62, v63 offset1:1
	ds_write2_b32 v177, v64, v65 offset1:1
	ds_write2_b32 v178, v58, v59 offset1:1
	ds_write2_b32 v179, v60, v61 offset1:1
	s_waitcnt lgkmcnt(0)
	ds_read2_b32 v[184:185], v150 offset1:8
	ds_read2_b32 v[186:187], v150 offset0:33 offset1:41
	ds_read2_b32 v[190:191], v150 offset0:66 offset1:74
	ds_read2_b32 v[192:193], v150 offset0:99 offset1:107
	v_mov_b32_e32 v180, v133
	ds_read2_b32 v[194:195], v150 offset0:132 offset1:140
	ds_read2_b32 v[196:197], v150 offset0:165 offset1:173
	s_waitcnt lgkmcnt(5)
	v_mul_f32_e32 v181, 0x42800000, v184
	s_waitcnt lgkmcnt(4)
	v_mul_f32_e32 v182, 0x42800000, v186
	v_cvt_pk_fp8_f32 v180, v181, v182
	s_waitcnt lgkmcnt(3)
	v_mul_f32_e32 v181, 0x42800000, v190
	s_waitcnt lgkmcnt(2)
	v_mul_f32_e32 v182, 0x42800000, v192
	ds_read2_b32 v[198:199], v150 offset0:198 offset1:206
	ds_read2_b32 v[200:201], v150 offset0:231 offset1:239
	v_cvt_pk_fp8_f32 v180, v181, v182 op_sel:[0,0,1]
	s_waitcnt lgkmcnt(3)
	v_mul_f32_e32 v182, 0x42800000, v194
	s_waitcnt lgkmcnt(2)
	v_mul_f32_e32 v183, 0x42800000, v196
	v_mov_b32_e32 v181, v133
	ds_read2_b32 v[202:203], v155 offset0:8 offset1:16
	ds_read2_b32 v[204:205], v155 offset0:41 offset1:49
	v_cvt_pk_fp8_f32 v181, v182, v183
	ds_read2_b32 v[206:207], v155 offset0:74 offset1:82
	ds_read2_b32 v[208:209], v155 offset0:107 offset1:115
	ds_read2_b32 v[210:211], v155 offset0:140 offset1:148
	ds_read2_b32 v[212:213], v155 offset0:173 offset1:181
	s_waitcnt lgkmcnt(7)
	v_mul_f32_e32 v182, 0x42800000, v198
	s_waitcnt lgkmcnt(6)
	v_mul_f32_e32 v183, 0x42800000, v200
	v_cvt_pk_fp8_f32 v181, v182, v183 op_sel:[0,0,1]
	s_waitcnt lgkmcnt(5)
	v_mul_f32_e32 v183, 0x42800000, v202
	s_waitcnt lgkmcnt(4)
	v_mul_f32_e32 v184, 0x42800000, v204
	v_mov_b32_e32 v182, v133
	ds_read2_b32 v[214:215], v155 offset0:206 offset1:214
	ds_read2_b32 v[216:217], v155 offset0:239 offset1:247
	v_cvt_pk_fp8_f32 v182, v183, v184
	s_waitcnt lgkmcnt(3)
	v_mul_f32_e32 v190, 0x42800000, v210
	s_waitcnt lgkmcnt(2)
	v_mul_f32_e32 v192, 0x42800000, v212
	v_mov_b32_e32 v183, v133
	v_cvt_pk_fp8_f32 v183, v190, v192
	v_mul_f32_e32 v184, 0x42800000, v206
	v_mul_f32_e32 v186, 0x42800000, v208
	v_cvt_pk_fp8_f32 v182, v184, v186 op_sel:[0,0,1]
	s_waitcnt lgkmcnt(1)
	v_mul_f32_e32 v184, 0x42800000, v214
	s_waitcnt lgkmcnt(0)
; #define LAS __attribute__((address_space(3)))
; #define LDS_WAIT() asm volatile("s_waitcnt lgkmcnt(0)" ::: "memory")
; template <int MODE>
; __device__ __forceinline__ void t128_store(const Ctx& c, const f32x4 (&v)[16], int K, int N, unsigned char* WT, int item) {
;     ...
;     const int cc = lane & 7;
; #pragma unroll
;     for (int j = 0; j < 4; ++j) { const int n = (lane >> 3) + 8 * j; const LAS float* s = scr + (16 * cc) * 33 + n; int w[4];
; #pragma unroll
;         for (int q = 0; q < 4; ++q) { int t = 0; t = __builtin_amdgcn_cvt_pk_fp8_f32(s[(4 * q) * 33] * WSCALE, s[(4 * q + 1) * 33] * WSCALE, t, false);
;             t = __builtin_amdgcn_cvt_pk_fp8_f32(s[(4 * q + 2) * 33] * WSCALE, s[(4 * q + 3) * 33] * WSCALE, t, true); w[q] = t; }
;         const int dr = drow_of<MODE>(n0 + n);
;         __builtin_nontemporal_store((u32x4){(unsigned)w[0], (unsigned)w[1], (unsigned)w[2], (unsigned)w[3]}, (u32x4*)(WT + (size_t)dr * K + k0 + 16 * cc)); }
;     LDS_WAIT(); asm volatile("" ::: "memory");
	v_mul_f32_e32 v186, 0x42800000, v216
	v_cvt_pk_fp8_f32 v183, v184, v186 op_sel:[0,0,1]
	v_mul_f32_e32 v185, 0x42800000, v185
	v_mul_f32_e32 v186, 0x42800000, v187
	v_mov_b32_e32 v184, v133
	v_cvt_pk_fp8_f32 v184, v185, v186
	v_mul_f32_e32 v186, 0x42800000, v191
	v_mul_f32_e32 v190, 0x42800000, v195
	v_mul_f32_e32 v191, 0x42800000, v197
	v_mov_b32_e32 v185, v133
	v_cvt_pk_fp8_f32 v185, v190, v191
	v_mul_f32_e32 v187, 0x42800000, v193
	v_cvt_pk_fp8_f32 v184, v186, v187 op_sel:[0,0,1]
	v_mul_f32_e32 v186, 0x42800000, v199
	v_mul_f32_e32 v187, 0x42800000, v201
	v_cvt_pk_fp8_f32 v185, v186, v187 op_sel:[0,0,1]
	v_mul_f32_e32 v187, 0x42800000, v203
	v_mul_f32_e32 v190, 0x42800000, v205
	v_mov_b32_e32 v186, v133
	v_cvt_pk_fp8_f32 v186, v187, v190
	v_mul_f32_e32 v192, 0x42800000, v211
	v_mul_f32_e32 v193, 0x42800000, v213
	v_mov_b32_e32 v187, v133
	v_cvt_pk_fp8_f32 v187, v192, v193
	s_add_i32 s20, s19, 0xffff7800
	v_mul_f32_e32 v190, 0x42800000, v207
	v_mul_f32_e32 v191, 0x42800000, v209
	s_lshr_b32 s42, s20, 11
	v_cvt_pk_fp8_f32 v186, v190, v191 op_sel:[0,0,1]
	v_mul_f32_e32 v190, 0x42800000, v215
	v_mul_f32_e32 v191, 0x42800000, v217
	s_lshl_b64 s[20:21], s[42:43], 23
	v_cvt_pk_fp8_f32 v187, v190, v191 op_sel:[0,0,1]
	v_lshl_add_u64 v[188:189], v[136:137], 0, s[20:21]
	ds_read2_b32 v[190:191], v150 offset0:16 offset1:24
	ds_read2_b32 v[192:193], v150 offset0:49 offset1:57
	v_lshl_add_u64 v[218:219], v[188:189], 0, v[138:139]
	global_store_dwordx4 v[218:219], v[180:183], off nt
	s_nop 1
	v_lshl_add_u64 v[180:181], v[188:189], 0, v[140:141]
	global_store_dwordx4 v[180:181], v[184:187], off nt
	ds_read2_b32 v[184:185], v150 offset0:82 offset1:90
	ds_read2_b32 v[186:187], v150 offset0:115 offset1:123
	s_waitcnt lgkmcnt(3)
	v_mul_f32_e32 v181, 0x42800000, v190
	s_waitcnt lgkmcnt(2)
	v_mul_f32_e32 v182, 0x42800000, v192
	v_mov_b32_e32 v180, v133
	ds_read2_b32 v[194:195], v150 offset0:148 offset1:156
	ds_read2_b32 v[196:197], v150 offset0:181 offset1:189
	v_cvt_pk_fp8_f32 v180, v181, v182
	s_waitcnt lgkmcnt(3)
	v_mul_f32_e32 v181, 0x42800000, v184
	s_waitcnt lgkmcnt(2)
	v_mul_f32_e32 v182, 0x42800000, v186
	ds_read2_b32 v[198:199], v150 offset0:214 offset1:222
	ds_read2_b32 v[200:201], v150 offset0:247 offset1:255
	v_cvt_pk_fp8_f32 v180, v181, v182 op_sel:[0,0,1]
	s_waitcnt lgkmcnt(3)
	v_mul_f32_e32 v182, 0x42800000, v194
	s_waitcnt lgkmcnt(2)
	v_mul_f32_e32 v183, 0x42800000, v196
	v_mov_b32_e32 v181, v133
	ds_read2_b32 v[202:203], v155 offset0:24 offset1:32
	ds_read2_b32 v[204:205], v155 offset0:57 offset1:65
	v_cvt_pk_fp8_f32 v181, v182, v183
	ds_read2_b32 v[206:207], v155 offset0:90 offset1:98
	ds_read2_b32 v[208:209], v155 offset0:123 offset1:131
	ds_read2_b32 v[210:211], v155 offset0:156 offset1:164
	ds_read2_b32 v[212:213], v155 offset0:189 offset1:197
	s_waitcnt lgkmcnt(7)
	v_mul_f32_e32 v182, 0x42800000, v198
	s_waitcnt lgkmcnt(6)
	v_mul_f32_e32 v183, 0x42800000, v200
	v_cvt_pk_fp8_f32 v181, v182, v183 op_sel:[0,0,1]
	s_waitcnt lgkmcnt(5)
	v_mul_f32_e32 v183, 0x42800000, v202
	s_waitcnt lgkmcnt(4)
	v_mul_f32_e32 v184, 0x42800000, v204
	v_mov_b32_e32 v182, v133
	ds_read2_b32 v[214:215], v155 offset0:222 offset1:230
	ds_read2_b32 v[216:217], v154 offset0:127 offset1:135
	v_cvt_pk_fp8_f32 v182, v183, v184
	s_waitcnt lgkmcnt(3)
	v_mul_f32_e32 v190, 0x42800000, v210
	s_waitcnt lgkmcnt(2)
	v_mul_f32_e32 v192, 0x42800000, v212
	v_mov_b32_e32 v183, v133
	v_cvt_pk_fp8_f32 v183, v190, v192
	v_mul_f32_e32 v184, 0x42800000, v206
	v_mul_f32_e32 v186, 0x42800000, v208
	v_cvt_pk_fp8_f32 v182, v184, v186 op_sel:[0,0,1]
	s_waitcnt lgkmcnt(1)
	v_mul_f32_e32 v184, 0x42800000, v214
	s_waitcnt lgkmcnt(0)
	v_mul_f32_e32 v186, 0x42800000, v216
	v_cvt_pk_fp8_f32 v183, v184, v186 op_sel:[0,0,1]
	v_mul_f32_e32 v186, 0x42800000, v191
	v_mul_f32_e32 v190, 0x42800000, v193
	v_mov_b32_e32 v184, v133
	v_cvt_pk_fp8_f32 v184, v186, v190
	v_mul_f32_e32 v186, 0x42800000, v185
	v_mul_f32_e32 v190, 0x42800000, v195
	v_mul_f32_e32 v191, 0x42800000, v197
	v_mov_b32_e32 v185, v133
	v_cvt_pk_fp8_f32 v185, v190, v191
	v_mul_f32_e32 v187, 0x42800000, v187
	v_cvt_pk_fp8_f32 v184, v186, v187 op_sel:[0,0,1]
	v_mul_f32_e32 v186, 0x42800000, v199
	v_mul_f32_e32 v187, 0x42800000, v201
	v_cvt_pk_fp8_f32 v185, v186, v187 op_sel:[0,0,1]
	v_mul_f32_e32 v187, 0x42800000, v203
	v_mul_f32_e32 v190, 0x42800000, v205
	v_mov_b32_e32 v186, v133
	v_cvt_pk_fp8_f32 v186, v187, v190
	v_mul_f32_e32 v192, 0x42800000, v211
	v_mul_f32_e32 v193, 0x42800000, v213
	v_mov_b32_e32 v187, v133
	v_cvt_pk_fp8_f32 v187, v192, v193
	v_mul_f32_e32 v190, 0x42800000, v207
	v_mul_f32_e32 v191, 0x42800000, v209
	v_cvt_pk_fp8_f32 v186, v190, v191 op_sel:[0,0,1]
	v_mul_f32_e32 v190, 0x42800000, v215
	v_mul_f32_e32 v191, 0x42800000, v217
	v_cvt_pk_fp8_f32 v187, v190, v191 op_sel:[0,0,1]
	v_lshl_add_u64 v[190:191], v[188:189], 0, v[142:143]
	global_store_dwordx4 v[190:191], v[180:183], off nt
	s_nop 1
	v_lshl_add_u64 v[180:181], v[188:189], 0, v[144:145]
	global_store_dwordx4 v[180:181], v[184:187], off nt
	s_waitcnt lgkmcnt(0)
	s_cbranch_execz .LBB0_291

; #define LAS __attribute__((address_space(3)))
; __device__ __forceinline__ unsigned stop_poll(const Ctx& c, const unsigned* p) {
;     volatile LAS unsigned* w = (volatile LAS unsigned*)(c.lds + STOPW_OFF);
;     if (c.wave == 0) { const unsigned v = __hip_atomic_load(p, __ATOMIC_RELAXED, __HIP_MEMORY_SCOPE_AGENT); if (c.lane == 0) *w = v; return (unsigned)__builtin_amdgcn_readfirstlane((int)v); }
;     return *w;
; __device__ __forceinline__ int conv_stream(const Ctx& c, int j, int first, int step, const unsigned* stop, const float* w_gu, const float* w_d, unsigned char* Wgu, unsigned char* Wd) {
;     ...
;         { const int i2 = i + step; const bool more = j + CONV_SLOTS * i2 < CONV_TOTAL && !(stop && stop_poll(c, stop) >= STOP_AT);
;           cs_load(j + CONV_SLOTS * (more ? i2 : i), c.lane, w_gu, w_d, va);
;           cs_store(c, j + CONV_SLOTS * i, vb, Wgu, Wd); i = i2; if (!more) break; }
.LBB0_274:
	s_cmp_gt_i32 s19, 0x17fff
	s_mov_b64 s[46:47], 0
	s_cbranch_scc1 .LBB0_282
	s_and_b64 vcc, exec, s[6:7]
	s_cbranch_vccz .LBB0_277
	s_waitcnt vmcnt(4)
	v_mov_b32_e32 v2, s18
	ds_read_b32 v2, v2
	s_mov_b64 s[44:45], 0
	s_waitcnt lgkmcnt(0)
	v_readfirstlane_b32 s20, v2

; #define LAS __attribute__((address_space(3)))
; #define LDS_WAIT() asm volatile("s_waitcnt lgkmcnt(0)" ::: "memory")
; __device__ __forceinline__ void t128_load(const float* W, int N, int item, int lane, f32x4 (&v)[16]) {
;     const int nblk = N / 32, kb = item / nblk, nb = item % nblk, k0 = 128 * kb, n0 = 32 * nb;
; #pragma unroll
;     for (int i = 0; i < 16; ++i) v[i] = __builtin_nontemporal_load((const f32x4*)(W + (size_t)(k0 + i * 8 + (lane >> 3)) * N + n0 + (lane & 7) * 4));
; }
; template <int MODE>
; __device__ __forceinline__ void t128_store(const Ctx& c, const f32x4 (&v)[16], int K, int N, unsigned char* WT, int item) {
;     LAS float* scr = (LAS float*)(c.lds + c.wave * CONV_SCR);
;     const int nblk = N / 32, kb = item / nblk, nb = item % nblk, k0 = 128 * kb, n0 = 32 * nb, lane = c.lane;
; #pragma unroll
;     for (int i = 0; i < 16; ++i) { LAS float* d = scr + (i * 8 + (lane >> 3)) * 33 + (lane & 7) * 4; d[0] = v[i].x; d[1] = v[i].y; d[2] = v[i].z; d[3] = v[i].w; }
;     LDS_WAIT(); asm volatile("" ::: "memory");
.LBB0_286:
	s_waitcnt vmcnt(4)
	v_or_b32_e32 v58, s21, v131
	v_ashrrev_i32_e32 v59, 31, v58
	v_lshlrev_b64 v[2:3], s46, v[58:59]
	v_add_u32_e32 v4, 8, v58
	v_add_u32_e32 v10, 16, v58
	v_add_u32_e32 v12, 24, v58
	v_add_u32_e32 v18, 32, v58
	v_add_u32_e32 v20, 40, v58
	v_add_u32_e32 v26, 48, v58
	v_add_u32_e32 v28, 56, v58
	v_add_u32_e32 v34, 64, v58
	v_add_u32_e32 v36, 0x48, v58
	v_add_u32_e32 v42, 0x50, v58
	v_add_u32_e32 v44, 0x58, v58
	v_add_u32_e32 v50, 0x60, v58
	v_add_u32_e32 v52, 0x68, v58
	v_add_u32_e32 v62, 0x70, v58
	v_add_u32_e32 v58, 0x78, v58
	v_ashrrev_i32_e32 v5, 31, v4
	v_ashrrev_i32_e32 v11, 31, v10
	v_ashrrev_i32_e32 v13, 31, v12
	v_ashrrev_i32_e32 v19, 31, v18
	v_ashrrev_i32_e32 v21, 31, v20
	v_ashrrev_i32_e32 v27, 31, v26
	v_ashrrev_i32_e32 v29, 31, v28
	v_ashrrev_i32_e32 v35, 31, v34
	v_ashrrev_i32_e32 v37, 31, v36
	v_ashrrev_i32_e32 v43, 31, v42
	v_ashrrev_i32_e32 v45, 31, v44
	v_ashrrev_i32_e32 v51, 31, v50
	v_ashrrev_i32_e32 v53, 31, v52
	v_ashrrev_i32_e32 v63, 31, v62
	v_ashrrev_i32_e32 v59, 31, v58
	v_lshl_add_u64 v[60:61], s[48:49], 0, v[132:133]
	v_lshlrev_b64 v[4:5], s46, v[4:5]
	v_lshlrev_b64 v[10:11], s46, v[10:11]
	v_lshlrev_b64 v[12:13], s46, v[12:13]
	v_lshlrev_b64 v[18:19], s46, v[18:19]
	v_lshlrev_b64 v[20:21], s46, v[20:21]
	v_lshlrev_b64 v[26:27], s46, v[26:27]
	v_lshlrev_b64 v[28:29], s46, v[28:29]
	v_lshlrev_b64 v[34:35], s46, v[34:35]
	v_lshlrev_b64 v[36:37], s46, v[36:37]
	v_lshlrev_b64 v[42:43], s46, v[42:43]
	v_lshlrev_b64 v[44:45], s46, v[44:45]
	v_lshlrev_b64 v[50:51], s46, v[50:51]
	v_lshlrev_b64 v[52:53], s46, v[52:53]
	v_lshlrev_b64 v[62:63], s46, v[62:63]
	v_lshlrev_b64 v[58:59], s46, v[58:59]
	v_lshl_add_u64 v[2:3], v[60:61], 0, v[2:3]
	v_lshl_add_u64 v[4:5], v[60:61], 0, v[4:5]
	v_lshl_add_u64 v[10:11], v[60:61], 0, v[10:11]
	v_lshl_add_u64 v[12:13], v[60:61], 0, v[12:13]
	v_lshl_add_u64 v[18:19], v[60:61], 0, v[18:19]
	v_lshl_add_u64 v[20:21], v[60:61], 0, v[20:21]
	v_lshl_add_u64 v[26:27], v[60:61], 0, v[26:27]
	v_lshl_add_u64 v[28:29], v[60:61], 0, v[28:29]
	v_lshl_add_u64 v[34:35], v[60:61], 0, v[34:35]
	v_lshl_add_u64 v[36:37], v[60:61], 0, v[36:37]
	v_lshl_add_u64 v[42:43], v[60:61], 0, v[42:43]
	v_lshl_add_u64 v[44:45], v[60:61], 0, v[44:45]
	v_lshl_add_u64 v[50:51], v[60:61], 0, v[50:51]
	v_lshl_add_u64 v[52:53], v[60:61], 0, v[52:53]
	v_lshl_add_u64 v[62:63], v[60:61], 0, v[62:63]
	v_lshl_add_u64 v[58:59], v[60:61], 0, v[58:59]
	global_load_dwordx4 v[6:9], v[2:3], off nt
	s_nop 0
	global_load_dwordx4 v[2:5], v[4:5], off nt
	s_nop 0
	global_load_dwordx4 v[14:17], v[10:11], off nt
	s_nop 0
	global_load_dwordx4 v[10:13], v[12:13], off nt
	s_nop 0
	global_load_dwordx4 v[22:25], v[18:19], off nt
	s_nop 0
	global_load_dwordx4 v[18:21], v[20:21], off nt
	s_nop 0
	global_load_dwordx4 v[30:33], v[26:27], off nt
	s_nop 0
	global_load_dwordx4 v[26:29], v[28:29], off nt
	s_nop 0
	global_load_dwordx4 v[38:41], v[34:35], off nt
	s_nop 0
	global_load_dwordx4 v[34:37], v[36:37], off nt
	s_nop 0
	global_load_dwordx4 v[46:49], v[42:43], off nt
	s_nop 0
	global_load_dwordx4 v[42:45], v[44:45], off nt
	s_nop 0
	global_load_dwordx4 v[54:57], v[50:51], off nt
	s_nop 0
	global_load_dwordx4 v[50:53], v[52:53], off nt
	s_nop 0
	global_load_dwordx4 v[62:65], v[62:63], off nt
	s_nop 0
	global_load_dwordx4 v[58:61], v[58:59], off nt
	s_cmpk_gt_i32 s24, 0x7fff
	s_mov_b64 s[46:47], -1
	s_cbranch_scc0 .LBB0_288
	ds_write2_b32 v146, v70, v71 offset1:1
	ds_write2_b32 v146, v72, v73 offset0:2 offset1:3
	ds_write2_b32 v151, v66, v67 offset1:1
	ds_write2_b32 v151, v68, v69 offset0:2 offset1:3
	ds_write2_b32 v152, v78, v79 offset1:1
	ds_write2_b32 v152, v80, v81 offset0:2 offset1:3
	ds_write2_b32 v153, v74, v75 offset1:1
	ds_write2_b32 v153, v76, v77 offset0:2 offset1:3
	ds_write2_b32 v156, v86, v87 offset1:1
	ds_write2_b32 v157, v88, v89 offset1:1
	ds_write2_b32 v158, v82, v83 offset1:1
	ds_write2_b32 v159, v84, v85 offset1:1
	ds_write2_b32 v160, v94, v95 offset1:1
	ds_write2_b32 v161, v96, v97 offset1:1
	ds_write2_b32 v162, v90, v91 offset1:1
	ds_write2_b32 v163, v92, v93 offset1:1
	ds_write2_b32 v164, v102, v103 offset1:1
	ds_write2_b32 v165, v104, v105 offset1:1
	ds_write2_b32 v166, v98, v99 offset1:1
	ds_write2_b32 v167, v100, v101 offset1:1
	ds_write2_b32 v168, v110, v111 offset1:1
	ds_write2_b32 v169, v112, v113 offset1:1
	ds_write2_b32 v170, v106, v107 offset1:1
	ds_write2_b32 v171, v108, v109 offset1:1
	ds_write2_b32 v172, v118, v119 offset1:1
	ds_write2_b32 v173, v120, v121 offset1:1
	ds_write2_b32 v174, v114, v115 offset1:1
	ds_write2_b32 v175, v116, v117 offset1:1
	ds_write2_b32 v176, v126, v127 offset1:1
	ds_write2_b32 v177, v128, v129 offset1:1
	ds_write2_b32 v178, v122, v123 offset1:1
	ds_write2_b32 v179, v124, v125 offset1:1
	s_waitcnt lgkmcnt(0)
	ds_read2_b32 v[184:185], v150 offset1:8
	ds_read2_b32 v[186:187], v150 offset0:33 offset1:41
	ds_read2_b32 v[190:191], v150 offset0:66 offset1:74
	ds_read2_b32 v[192:193], v150 offset0:99 offset1:107
	v_mov_b32_e32 v180, v133
	ds_read2_b32 v[194:195], v150 offset0:132 offset1:140
	ds_read2_b32 v[196:197], v150 offset0:165 offset1:173
	s_waitcnt lgkmcnt(5)
	v_mul_f32_e32 v132, 0x42800000, v184
	s_waitcnt lgkmcnt(4)
	v_mul_f32_e32 v181, 0x42800000, v186
	v_cvt_pk_fp8_f32 v180, v132, v181
	s_waitcnt lgkmcnt(3)
	v_mul_f32_e32 v132, 0x42800000, v190
	s_waitcnt lgkmcnt(2)
	v_mul_f32_e32 v181, 0x42800000, v192
	ds_read2_b32 v[198:199], v150 offset0:198 offset1:206
	ds_read2_b32 v[200:201], v150 offset0:231 offset1:239
	v_cvt_pk_fp8_f32 v180, v132, v181 op_sel:[0,0,1]
	s_waitcnt lgkmcnt(3)
	v_mul_f32_e32 v132, 0x42800000, v194
	s_waitcnt lgkmcnt(2)
; #define LAS __attribute__((address_space(3)))
; #define LDS_WAIT() asm volatile("s_waitcnt lgkmcnt(0)" ::: "memory")
; template <int MODE>
; __device__ __forceinline__ void t128_store(const Ctx& c, const f32x4 (&v)[16], int K, int N, unsigned char* WT, int item) {
;     ...
;     const int cc = lane & 7;
; #pragma unroll
;     for (int j = 0; j < 4; ++j) { const int n = (lane >> 3) + 8 * j; const LAS float* s = scr + (16 * cc) * 33 + n; int w[4];
; #pragma unroll
;         for (int q = 0; q < 4; ++q) { int t = 0; t = __builtin_amdgcn_cvt_pk_fp8_f32(s[(4 * q) * 33] * WSCALE, s[(4 * q + 1) * 33] * WSCALE, t, false);
;             t = __builtin_amdgcn_cvt_pk_fp8_f32(s[(4 * q + 2) * 33] * WSCALE, s[(4 * q + 3) * 33] * WSCALE, t, true); w[q] = t; }
;         const int dr = drow_of<MODE>(n0 + n);
;         __builtin_nontemporal_store((u32x4){(unsigned)w[0], (unsigned)w[1], (unsigned)w[2], (unsigned)w[3]}, (u32x4*)(WT + (size_t)dr * K + k0 + 16 * cc)); }
;     LDS_WAIT(); asm volatile("" ::: "memory");
	v_mul_f32_e32 v182, 0x42800000, v196
	v_mov_b32_e32 v181, v133
	ds_read2_b32 v[202:203], v155 offset0:8 offset1:16
	ds_read2_b32 v[204:205], v155 offset0:41 offset1:49
	v_cvt_pk_fp8_f32 v181, v132, v182
	ds_read2_b32 v[206:207], v155 offset0:74 offset1:82
	ds_read2_b32 v[208:209], v155 offset0:107 offset1:115
	ds_read2_b32 v[210:211], v155 offset0:140 offset1:148
	ds_read2_b32 v[212:213], v155 offset0:173 offset1:181
	s_waitcnt lgkmcnt(7)
	v_mul_f32_e32 v132, 0x42800000, v198
	s_waitcnt lgkmcnt(6)
	v_mul_f32_e32 v182, 0x42800000, v200
	v_cvt_pk_fp8_f32 v181, v132, v182 op_sel:[0,0,1]
	s_waitcnt lgkmcnt(5)
	v_mul_f32_e32 v132, 0x42800000, v202
	s_waitcnt lgkmcnt(4)
	v_mul_f32_e32 v183, 0x42800000, v204
	v_mov_b32_e32 v182, v133
	ds_read2_b32 v[214:215], v155 offset0:206 offset1:214
	ds_read2_b32 v[216:217], v155 offset0:239 offset1:247
	v_cvt_pk_fp8_f32 v182, v132, v183
	s_waitcnt lgkmcnt(3)
	v_mul_f32_e32 v186, 0x42800000, v210
	s_waitcnt lgkmcnt(2)
	v_mul_f32_e32 v190, 0x42800000, v212
	v_mov_b32_e32 v183, v133
	v_cvt_pk_fp8_f32 v183, v186, v190
	v_mul_f32_e32 v132, 0x42800000, v206
	v_mul_f32_e32 v184, 0x42800000, v208
	v_cvt_pk_fp8_f32 v182, v132, v184 op_sel:[0,0,1]
	s_waitcnt lgkmcnt(1)
	v_mul_f32_e32 v132, 0x42800000, v214
	s_waitcnt lgkmcnt(0)
	v_mul_f32_e32 v184, 0x42800000, v216
	v_cvt_pk_fp8_f32 v183, v132, v184 op_sel:[0,0,1]
	v_mul_f32_e32 v132, 0x42800000, v185
	v_mul_f32_e32 v185, 0x42800000, v187
	v_mov_b32_e32 v184, v133
	v_cvt_pk_fp8_f32 v184, v132, v185
	v_mul_f32_e32 v187, 0x42800000, v195
	v_mul_f32_e32 v190, 0x42800000, v197
	v_mov_b32_e32 v185, v133
	v_cvt_pk_fp8_f32 v185, v187, v190
	v_mul_f32_e32 v132, 0x42800000, v191
	v_mul_f32_e32 v186, 0x42800000, v193
	v_cvt_pk_fp8_f32 v184, v132, v186 op_sel:[0,0,1]
	v_mul_f32_e32 v132, 0x42800000, v199
	v_mul_f32_e32 v186, 0x42800000, v201
	s_add_i32 s20, s19, 0xffff7c00
	v_cvt_pk_fp8_f32 v185, v132, v186 op_sel:[0,0,1]
	v_mul_f32_e32 v132, 0x42800000, v203
	v_mul_f32_e32 v187, 0x42800000, v205
	v_mov_b32_e32 v186, v133
	s_lshr_b32 s42, s20, 11
	v_cvt_pk_fp8_f32 v186, v132, v187
	v_mul_f32_e32 v191, 0x42800000, v211
	v_mul_f32_e32 v192, 0x42800000, v213
	v_mov_b32_e32 v187, v133
	s_lshl_b64 s[20:21], s[42:43], 23
	v_cvt_pk_fp8_f32 v187, v191, v192
	s_add_u32 s20, s38, s20
	s_addc_u32 s21, s39, s21
	s_and_b32 s25, s24, 0x780
	v_mul_f32_e32 v132, 0x42800000, v207
	v_mul_f32_e32 v190, 0x42800000, v209
	s_add_u32 s20, s20, s25
	v_cvt_pk_fp8_f32 v186, v132, v190 op_sel:[0,0,1]
	v_mul_f32_e32 v132, 0x42800000, v215
	v_mul_f32_e32 v190, 0x42800000, v217
	s_addc_u32 s21, s21, 0
	v_cvt_pk_fp8_f32 v187, v132, v190 op_sel:[0,0,1]
	v_lshl_add_u64 v[188:189], s[20:21], 0, v[134:135]
	ds_read2_b32 v[190:191], v150 offset0:16 offset1:24
	ds_read2_b32 v[192:193], v150 offset0:49 offset1:57
	v_lshl_add_u64 v[218:219], v[188:189], 0, v[138:139]
	global_store_dwordx4 v[218:219], v[180:183], off nt
	s_mov_b64 s[46:47], 0
	s_waitcnt lgkmcnt(1)
	v_mul_f32_e32 v132, 0x42800000, v190
	v_lshl_add_u64 v[180:181], v[188:189], 0, v[140:141]
	global_store_dwordx4 v[180:181], v[184:187], off nt
	ds_read2_b32 v[184:185], v150 offset0:82 offset1:90
	ds_read2_b32 v[186:187], v150 offset0:115 offset1:123
	s_waitcnt lgkmcnt(2)
	v_mul_f32_e32 v181, 0x42800000, v192
	v_mov_b32_e32 v180, v133
	ds_read2_b32 v[194:195], v150 offset0:148 offset1:156
	ds_read2_b32 v[196:197], v150 offset0:181 offset1:189
	v_cvt_pk_fp8_f32 v180, v132, v181
	s_waitcnt lgkmcnt(3)
	v_mul_f32_e32 v132, 0x42800000, v184
	s_waitcnt lgkmcnt(2)
	v_mul_f32_e32 v181, 0x42800000, v186
	ds_read2_b32 v[198:199], v150 offset0:214 offset1:222
	ds_read2_b32 v[200:201], v150 offset0:247 offset1:255
	v_cvt_pk_fp8_f32 v180, v132, v181 op_sel:[0,0,1]
	s_waitcnt lgkmcnt(3)
	v_mul_f32_e32 v132, 0x42800000, v194
	s_waitcnt lgkmcnt(2)
	v_mul_f32_e32 v182, 0x42800000, v196
	v_mov_b32_e32 v181, v133
	ds_read2_b32 v[202:203], v155 offset0:24 offset1:32
	ds_read2_b32 v[204:205], v155 offset0:57 offset1:65
	v_cvt_pk_fp8_f32 v181, v132, v182
	ds_read2_b32 v[206:207], v155 offset0:90 offset1:98
	ds_read2_b32 v[208:209], v155 offset0:123 offset1:131
	ds_read2_b32 v[210:211], v155 offset0:156 offset1:164
	ds_read2_b32 v[212:213], v155 offset0:189 offset1:197
	s_waitcnt lgkmcnt(7)
	v_mul_f32_e32 v132, 0x42800000, v198
	s_waitcnt lgkmcnt(6)
	v_mul_f32_e32 v182, 0x42800000, v200
	v_cvt_pk_fp8_f32 v181, v132, v182 op_sel:[0,0,1]
	s_waitcnt lgkmcnt(5)
	v_mul_f32_e32 v132, 0x42800000, v202
	s_waitcnt lgkmcnt(4)
	v_mul_f32_e32 v183, 0x42800000, v204
	v_mov_b32_e32 v182, v133
	ds_read2_b32 v[214:215], v155 offset0:222 offset1:230
	ds_read2_b32 v[216:217], v154 offset0:127 offset1:135
	v_cvt_pk_fp8_f32 v182, v132, v183
	s_waitcnt lgkmcnt(3)
	v_mul_f32_e32 v186, 0x42800000, v210
	s_waitcnt lgkmcnt(2)
	v_mul_f32_e32 v190, 0x42800000, v212
	v_mov_b32_e32 v183, v133
	v_cvt_pk_fp8_f32 v183, v186, v190
	v_mul_f32_e32 v132, 0x42800000, v206
	v_mul_f32_e32 v184, 0x42800000, v208
	v_cvt_pk_fp8_f32 v182, v132, v184 op_sel:[0,0,1]
	s_waitcnt lgkmcnt(1)
	v_mul_f32_e32 v132, 0x42800000, v214
	s_waitcnt lgkmcnt(0)
	v_mul_f32_e32 v184, 0x42800000, v216
	v_cvt_pk_fp8_f32 v183, v132, v184 op_sel:[0,0,1]
	v_mul_f32_e32 v132, 0x42800000, v191
	v_mul_f32_e32 v186, 0x42800000, v193
	v_mov_b32_e32 v184, v133
	v_cvt_pk_fp8_f32 v184, v132, v186
	v_mul_f32_e32 v132, 0x42800000, v185
	v_mul_f32_e32 v186, 0x42800000, v187
	v_mul_f32_e32 v187, 0x42800000, v195
	v_mul_f32_e32 v190, 0x42800000, v197
	v_mov_b32_e32 v185, v133
	v_cvt_pk_fp8_f32 v185, v187, v190
	v_cvt_pk_fp8_f32 v184, v132, v186 op_sel:[0,0,1]
	v_mul_f32_e32 v132, 0x42800000, v199
	v_mul_f32_e32 v186, 0x42800000, v201
	v_cvt_pk_fp8_f32 v185, v132, v186 op_sel:[0,0,1]
	v_mul_f32_e32 v132, 0x42800000, v203
	v_mul_f32_e32 v187, 0x42800000, v205
	v_mov_b32_e32 v186, v133
	v_cvt_pk_fp8_f32 v186, v132, v187
	v_mul_f32_e32 v191, 0x42800000, v211
	v_mul_f32_e32 v192, 0x42800000, v213
	v_mov_b32_e32 v187, v133
	v_cvt_pk_fp8_f32 v187, v191, v192
	v_mul_f32_e32 v132, 0x42800000, v207
	v_mul_f32_e32 v190, 0x42800000, v209
	v_cvt_pk_fp8_f32 v186, v132, v190 op_sel:[0,0,1]
	v_mul_f32_e32 v132, 0x42800000, v215
	v_mul_f32_e32 v190, 0x42800000, v217
	v_cvt_pk_fp8_f32 v187, v132, v190 op_sel:[0,0,1]
	v_lshl_add_u64 v[190:191], v[188:189], 0, v[142:143]
	global_store_dwordx4 v[190:191], v[180:183], off nt
	s_nop 1
	v_lshl_add_u64 v[180:181], v[188:189], 0, v[144:145]
	global_store_dwordx4 v[180:181], v[184:187], off nt
	s_waitcnt lgkmcnt(0)

; #define LAS __attribute__((address_space(3)))
; #define LDS_WAIT() asm volatile("s_waitcnt lgkmcnt(0)" ::: "memory")
; template <int MODE>
; __device__ __forceinline__ void t128_store(const Ctx& c, const f32x4 (&v)[16], int K, int N, unsigned char* WT, int item) {
;     LAS float* scr = (LAS float*)(c.lds + c.wave * CONV_SCR);
;     const int nblk = N / 32, kb = item / nblk, nb = item % nblk, k0 = 128 * kb, n0 = 32 * nb, lane = c.lane;
; #pragma unroll
;     for (int i = 0; i < 16; ++i) { LAS float* d = scr + (i * 8 + (lane >> 3)) * 33 + (lane & 7) * 4; d[0] = v[i].x; d[1] = v[i].y; d[2] = v[i].z; d[3] = v[i].w; }
;     LDS_WAIT(); asm volatile("" ::: "memory");
;     const int cc = lane & 7;
; #pragma unroll
;     for (int j = 0; j < 4; ++j) { const int n = (lane >> 3) + 8 * j; const LAS float* s = scr + (16 * cc) * 33 + n; int w[4];
; #pragma unroll
;         for (int q = 0; q < 4; ++q) { int t = 0; t = __builtin_amdgcn_cvt_pk_fp8_f32(s[(4 * q) * 33] * WSCALE, s[(4 * q + 1) * 33] * WSCALE, t, false);
;             t = __builtin_amdgcn_cvt_pk_fp8_f32(s[(4 * q + 2) * 33] * WSCALE, s[(4 * q + 3) * 33] * WSCALE, t, true); w[q] = t; }
;         const int dr = drow_of<MODE>(n0 + n);
;         __builtin_nontemporal_store((u32x4){(unsigned)w[0], (unsigned)w[1], (unsigned)w[2], (unsigned)w[3]}, (u32x4*)(WT + (size_t)dr * K + k0 + 16 * cc)); }
;     LDS_WAIT(); asm volatile("" ::: "memory");
; }
.LBB0_291:
	s_nop 0
	ds_write2_b32 v146, v6, v7 offset1:1
	ds_write2_b32 v146, v8, v9 offset0:2 offset1:3
	ds_write2_b32 v151, v2, v3 offset1:1
	ds_write2_b32 v151, v4, v5 offset0:2 offset1:3
	ds_write2_b32 v152, v14, v15 offset1:1
	ds_write2_b32 v152, v16, v17 offset0:2 offset1:3
	ds_write2_b32 v153, v10, v11 offset1:1
	ds_write2_b32 v153, v12, v13 offset0:2 offset1:3
	ds_write2_b32 v156, v22, v23 offset1:1
	ds_write2_b32 v157, v24, v25 offset1:1
	ds_write2_b32 v158, v18, v19 offset1:1
	ds_write2_b32 v159, v20, v21 offset1:1
	ds_write2_b32 v160, v30, v31 offset1:1
	ds_write2_b32 v161, v32, v33 offset1:1
	ds_write2_b32 v162, v26, v27 offset1:1
	ds_write2_b32 v163, v28, v29 offset1:1
	ds_write2_b32 v164, v38, v39 offset1:1
	ds_write2_b32 v165, v40, v41 offset1:1
	ds_write2_b32 v166, v34, v35 offset1:1
	ds_write2_b32 v167, v36, v37 offset1:1
	ds_write2_b32 v168, v46, v47 offset1:1
	ds_write2_b32 v169, v48, v49 offset1:1
	ds_write2_b32 v170, v42, v43 offset1:1
	ds_write2_b32 v171, v44, v45 offset1:1
	ds_write2_b32 v172, v54, v55 offset1:1
	ds_write2_b32 v173, v56, v57 offset1:1
	ds_write2_b32 v174, v50, v51 offset1:1
	ds_write2_b32 v175, v52, v53 offset1:1
	ds_write2_b32 v176, v62, v63 offset1:1
	ds_write2_b32 v177, v64, v65 offset1:1
	ds_write2_b32 v178, v58, v59 offset1:1
	ds_write2_b32 v179, v60, v61 offset1:1
	s_waitcnt lgkmcnt(0)
	ds_read2_b32 v[6:7], v150 offset1:8
	ds_read2_b32 v[8:9], v150 offset0:33 offset1:41
	ds_read2_b32 v[12:13], v150 offset0:66 offset1:74
	ds_read2_b32 v[14:15], v150 offset0:99 offset1:107
	s_ashr_i32 s20, s26, 31
	v_mov_b32_e32 v2, v133
	s_waitcnt lgkmcnt(3)
	v_mul_f32_e32 v3, 0x42800000, v6
	s_waitcnt lgkmcnt(2)
	v_mul_f32_e32 v4, 0x42800000, v8
	ds_read2_b32 v[16:17], v150 offset0:132 offset1:140
	ds_read2_b32 v[18:19], v150 offset0:165 offset1:173
	s_lshr_b32 s20, s20, 22
	v_cvt_pk_fp8_f32 v2, v3, v4
	s_add_i32 s27, s26, s20
	s_ashr_i32 s20, s27, 10
	s_ashr_i32 s21, s20, 31
	s_waitcnt lgkmcnt(3)
	v_mul_f32_e32 v3, 0x42800000, v12
	s_waitcnt lgkmcnt(2)
	v_mul_f32_e32 v4, 0x42800000, v14
	ds_read2_b32 v[20:21], v150 offset0:198 offset1:206
	ds_read2_b32 v[22:23], v150 offset0:231 offset1:239
	s_lshl_b64 s[20:21], s[20:21], 22
	v_cvt_pk_fp8_f32 v2, v3, v4 op_sel:[0,0,1]
	s_waitcnt lgkmcnt(3)
	v_mul_f32_e32 v4, 0x42800000, v16
	s_waitcnt lgkmcnt(2)
	v_mul_f32_e32 v5, 0x42800000, v18
	v_mov_b32_e32 v3, v133
	ds_read2_b32 v[24:25], v155 offset0:8 offset1:16
	ds_read2_b32 v[26:27], v155 offset0:41 offset1:49
	s_add_u32 s42, s9, s20
	v_cvt_pk_fp8_f32 v3, v4, v5
	ds_read2_b32 v[28:29], v155 offset0:74 offset1:82
	ds_read2_b32 v[30:31], v155 offset0:107 offset1:115
	ds_read2_b32 v[32:33], v155 offset0:140 offset1:148
	ds_read2_b32 v[34:35], v155 offset0:173 offset1:181
	s_addc_u32 s21, s14, s21
	s_and_b32 s20, s27, 0xfc00
	s_sub_i32 s20, s26, s20
	s_sext_i32_i16 s26, s20
	s_waitcnt lgkmcnt(7)
	v_mul_f32_e32 v4, 0x42800000, v20
	s_waitcnt lgkmcnt(6)
	v_mul_f32_e32 v5, 0x42800000, v22
	s_bfe_u32 s26, s26, 0x60019
	v_cvt_pk_fp8_f32 v3, v4, v5 op_sel:[0,0,1]
	s_waitcnt lgkmcnt(5)
	v_mul_f32_e32 v5, 0x42800000, v24
	s_waitcnt lgkmcnt(4)
	v_mul_f32_e32 v6, 0x42800000, v26
	v_mov_b32_e32 v4, v133
	ds_read2_b32 v[36:37], v155 offset0:206 offset1:214
	ds_read2_b32 v[38:39], v155 offset0:239 offset1:247
	s_add_i32 s26, s20, s26
	v_cvt_pk_fp8_f32 v4, v5, v6
	s_waitcnt lgkmcnt(3)
	v_mul_f32_e32 v12, 0x42800000, v32
	s_waitcnt lgkmcnt(2)
	v_mul_f32_e32 v14, 0x42800000, v34
	v_mov_b32_e32 v5, v133
	s_sext_i32_i16 s27, s26
	s_and_b32 s26, s26, 0xffc0
	v_cvt_pk_fp8_f32 v5, v12, v14
	s_sub_i32 s20, s20, s26
	s_lshl_b32 s26, s27, 1
	s_and_b32 s26, s26, 0xffffff80
	s_sext_i32_i16 s20, s20
	v_mul_f32_e32 v6, 0x42800000, v28
	v_mul_f32_e32 v8, 0x42800000, v30
	s_lshl_b32 s20, s20, 5
	s_ashr_i32 s27, s26, 31
	v_cvt_pk_fp8_f32 v4, v6, v8 op_sel:[0,0,1]
	s_waitcnt lgkmcnt(1)
	v_mul_f32_e32 v6, 0x42800000, v36
	s_waitcnt lgkmcnt(0)
; #define LAS __attribute__((address_space(3)))
; #define LDS_WAIT() asm volatile("s_waitcnt lgkmcnt(0)" ::: "memory")
; template <int MODE>
; __device__ __forceinline__ void t128_store(const Ctx& c, const f32x4 (&v)[16], int K, int N, unsigned char* WT, int item) {
;     ...
;     const int cc = lane & 7;
; #pragma unroll
;     for (int j = 0; j < 4; ++j) { const int n = (lane >> 3) + 8 * j; const LAS float* s = scr + (16 * cc) * 33 + n; int w[4];
; #pragma unroll
;         for (int q = 0; q < 4; ++q) { int t = 0; t = __builtin_amdgcn_cvt_pk_fp8_f32(s[(4 * q) * 33] * WSCALE, s[(4 * q + 1) * 33] * WSCALE, t, false);
;             t = __builtin_amdgcn_cvt_pk_fp8_f32(s[(4 * q + 2) * 33] * WSCALE, s[(4 * q + 3) * 33] * WSCALE, t, true); w[q] = t; }
;         const int dr = drow_of<MODE>(n0 + n);
;         __builtin_nontemporal_store((u32x4){(unsigned)w[0], (unsigned)w[1], (unsigned)w[2], (unsigned)w[3]}, (u32x4*)(WT + (size_t)dr * K + k0 + 16 * cc)); }
;     LDS_WAIT(); asm volatile("" ::: "memory");
; }
; __device__ __forceinline__ int conv_stream(const Ctx& c, int j, int first, int step, const unsigned* stop, const float* w_gu, const float* w_d, unsigned char* Wgu, unsigned char* Wd) {
;     ...
;         { const int i2 = i + step; const bool more = j + CONV_SLOTS * i2 < CONV_TOTAL && !(stop && stop_poll(c, stop) >= STOP_AT);
;           cs_load(j + CONV_SLOTS * (more ? i2 : i), c.lane, w_gu, w_d, va);
;           cs_store(c, j + CONV_SLOTS * i, vb, Wgu, Wd); i = i2; if (!more) break; }
;     }
	v_mul_f32_e32 v8, 0x42800000, v38
	s_add_u32 s26, s42, s26
	v_cvt_pk_fp8_f32 v5, v6, v8 op_sel:[0,0,1]
	v_or_b32_e32 v40, s20, v131
	s_addc_u32 s27, s21, s27
	v_ashrrev_i32_e32 v41, 31, v40
	v_lshl_add_u64 v[10:11], s[26:27], 0, v[134:135]
	v_lshlrev_b64 v[40:41], 11, v[40:41]
	v_lshl_add_u64 v[40:41], v[10:11], 0, v[40:41]
	global_store_dwordx4 v[40:41], v[2:5], off nt
	v_mul_f32_e32 v6, 0x42800000, v17
	v_mul_f32_e32 v8, 0x42800000, v33
	v_mul_f32_e32 v3, 0x42800000, v7
	v_mul_f32_e32 v4, 0x42800000, v9
	v_mov_b32_e32 v2, v133
	v_cvt_pk_fp8_f32 v2, v3, v4
	v_mul_f32_e32 v7, 0x42800000, v19
	v_mov_b32_e32 v3, v133
	v_cvt_pk_fp8_f32 v3, v6, v7
	v_mul_f32_e32 v4, 0x42800000, v13
	v_mul_f32_e32 v5, 0x42800000, v15
	v_cvt_pk_fp8_f32 v2, v4, v5 op_sel:[0,0,1]
	v_mul_f32_e32 v4, 0x42800000, v21
	v_mul_f32_e32 v5, 0x42800000, v23
	v_cvt_pk_fp8_f32 v3, v4, v5 op_sel:[0,0,1]
	v_mul_f32_e32 v5, 0x42800000, v25
	v_mul_f32_e32 v6, 0x42800000, v27
	v_mov_b32_e32 v4, v133
	v_cvt_pk_fp8_f32 v4, v5, v6
	v_mul_f32_e32 v9, 0x42800000, v35
	v_mov_b32_e32 v5, v133
	v_cvt_pk_fp8_f32 v5, v8, v9
	v_mul_f32_e32 v6, 0x42800000, v29
	v_mul_f32_e32 v7, 0x42800000, v31
	v_cvt_pk_fp8_f32 v4, v6, v7 op_sel:[0,0,1]
	v_mul_f32_e32 v6, 0x42800000, v37
	v_mul_f32_e32 v7, 0x42800000, v39
	v_cvt_pk_fp8_f32 v5, v6, v7 op_sel:[0,0,1]
	v_or_b32_e32 v6, s20, v147
	v_ashrrev_i32_e32 v7, 31, v6
	ds_read2_b32 v[8:9], v150 offset0:16 offset1:24
	ds_read2_b32 v[12:13], v150 offset0:49 offset1:57
	v_lshlrev_b64 v[6:7], 11, v[6:7]
	v_lshl_add_u64 v[6:7], v[10:11], 0, v[6:7]
	global_store_dwordx4 v[6:7], v[2:5], off nt
	ds_read2_b32 v[6:7], v150 offset0:82 offset1:90
	ds_read2_b32 v[14:15], v150 offset0:115 offset1:123
	s_waitcnt lgkmcnt(3)
	v_mul_f32_e32 v3, 0x42800000, v8
	s_waitcnt lgkmcnt(2)
	v_mul_f32_e32 v4, 0x42800000, v12
	v_mov_b32_e32 v2, v133
	ds_read2_b32 v[16:17], v150 offset0:148 offset1:156
	ds_read2_b32 v[18:19], v150 offset0:181 offset1:189
	v_cvt_pk_fp8_f32 v2, v3, v4
	s_waitcnt lgkmcnt(3)
	v_mul_f32_e32 v3, 0x42800000, v6
	s_waitcnt lgkmcnt(2)
	v_mul_f32_e32 v4, 0x42800000, v14
	ds_read2_b32 v[20:21], v150 offset0:214 offset1:222
	ds_read2_b32 v[22:23], v150 offset0:247 offset1:255
	v_cvt_pk_fp8_f32 v2, v3, v4 op_sel:[0,0,1]
	s_waitcnt lgkmcnt(3)
	v_mul_f32_e32 v4, 0x42800000, v16
	s_waitcnt lgkmcnt(2)
	v_mul_f32_e32 v5, 0x42800000, v18
	v_mov_b32_e32 v3, v133
	ds_read2_b32 v[24:25], v155 offset0:24 offset1:32
	ds_read2_b32 v[26:27], v155 offset0:57 offset1:65
	v_cvt_pk_fp8_f32 v3, v4, v5
	ds_read2_b32 v[28:29], v155 offset0:90 offset1:98
	ds_read2_b32 v[30:31], v155 offset0:123 offset1:131
	ds_read2_b32 v[32:33], v155 offset0:156 offset1:164
	ds_read2_b32 v[34:35], v155 offset0:189 offset1:197
	s_waitcnt lgkmcnt(7)
	v_mul_f32_e32 v4, 0x42800000, v20
	s_waitcnt lgkmcnt(6)
	v_mul_f32_e32 v5, 0x42800000, v22
	v_cvt_pk_fp8_f32 v3, v4, v5 op_sel:[0,0,1]
	s_waitcnt lgkmcnt(5)
	v_mul_f32_e32 v5, 0x42800000, v24
	s_waitcnt lgkmcnt(4)
	v_mul_f32_e32 v6, 0x42800000, v26
	v_mov_b32_e32 v4, v133
	ds_read2_b32 v[36:37], v155 offset0:222 offset1:230
	ds_read2_b32 v[38:39], v154 offset0:127 offset1:135
	v_cvt_pk_fp8_f32 v4, v5, v6
	s_waitcnt lgkmcnt(3)
	v_mul_f32_e32 v12, 0x42800000, v32
	s_waitcnt lgkmcnt(2)
	v_mul_f32_e32 v14, 0x42800000, v34
	v_mov_b32_e32 v5, v133
	v_cvt_pk_fp8_f32 v5, v12, v14
	v_mul_f32_e32 v6, 0x42800000, v28
	v_mul_f32_e32 v8, 0x42800000, v30
	v_cvt_pk_fp8_f32 v4, v6, v8 op_sel:[0,0,1]
	s_waitcnt lgkmcnt(1)
	v_mul_f32_e32 v6, 0x42800000, v36
	s_waitcnt lgkmcnt(0)
	v_mul_f32_e32 v8, 0x42800000, v38
	v_cvt_pk_fp8_f32 v5, v6, v8 op_sel:[0,0,1]
	v_or_b32_e32 v40, s20, v148
	v_ashrrev_i32_e32 v41, 31, v40
	v_lshlrev_b64 v[40:41], 11, v[40:41]
	v_lshl_add_u64 v[40:41], v[10:11], 0, v[40:41]
	global_store_dwordx4 v[40:41], v[2:5], off nt
	v_mul_f32_e32 v6, 0x42800000, v17
	v_mul_f32_e32 v8, 0x42800000, v33
	v_mul_f32_e32 v3, 0x42800000, v9
	v_mul_f32_e32 v4, 0x42800000, v13
	v_mov_b32_e32 v2, v133
	v_cvt_pk_fp8_f32 v2, v3, v4
	v_mul_f32_e32 v4, 0x42800000, v7
	v_mul_f32_e32 v7, 0x42800000, v19
	v_mov_b32_e32 v3, v133
	v_cvt_pk_fp8_f32 v3, v6, v7
	v_mul_f32_e32 v5, 0x42800000, v15
	v_cvt_pk_fp8_f32 v2, v4, v5 op_sel:[0,0,1]
	v_mul_f32_e32 v4, 0x42800000, v21
	v_mul_f32_e32 v5, 0x42800000, v23
	v_cvt_pk_fp8_f32 v3, v4, v5 op_sel:[0,0,1]
	v_mul_f32_e32 v5, 0x42800000, v25
	v_mul_f32_e32 v6, 0x42800000, v27
	v_mov_b32_e32 v4, v133
	v_cvt_pk_fp8_f32 v4, v5, v6
	v_mul_f32_e32 v9, 0x42800000, v35
	v_mov_b32_e32 v5, v133
	v_cvt_pk_fp8_f32 v5, v8, v9
	v_mul_f32_e32 v6, 0x42800000, v29
	v_mul_f32_e32 v7, 0x42800000, v31
	v_cvt_pk_fp8_f32 v4, v6, v7 op_sel:[0,0,1]
	v_mul_f32_e32 v6, 0x42800000, v37
	v_mul_f32_e32 v7, 0x42800000, v39
	v_cvt_pk_fp8_f32 v5, v6, v7 op_sel:[0,0,1]
	v_or_b32_e32 v6, s20, v149
	v_ashrrev_i32_e32 v7, 31, v6
	v_lshlrev_b64 v[6:7], 11, v[6:7]
	v_lshl_add_u64 v[6:7], v[10:11], 0, v[6:7]
	global_store_dwordx4 v[6:7], v[2:5], off nt
	s_waitcnt lgkmcnt(0)
	s_andn2_b64 vcc, exec, s[44:45]
	s_mov_b64 s[44:45], -1
	s_cbranch_vccz .LBB0_274

; __device__ __forceinline__ int conv_stream(const Ctx& c, int j, int first, int step, const unsigned* stop, const float* w_gu, const float* w_d, unsigned char* Wgu, unsigned char* Wd) {
;     ...
;         { const int i2 = i + step; const bool more = j + CONV_SLOTS * i2 < CONV_TOTAL && !(stop && stop_poll(c, stop) >= STOP_AT);
;           cs_load(j + CONV_SLOTS * (more ? i2 : i), c.lane, w_gu, w_d, vb);
;           cs_store(c, j + CONV_SLOTS * i, va, Wgu, Wd); i = i2; if (!more) break; }
;         { const int i2 = i + step; const bool more = j + CONV_SLOTS * i2 < CONV_TOTAL && !(stop && stop_poll(c, stop) >= STOP_AT);
;           cs_load(j + CONV_SLOTS * (more ? i2 : i), c.lane, w_gu, w_d, va);
;           cs_store(c, j + CONV_SLOTS * i, vb, Wgu, Wd); i = i2; if (!more) break; }
;     }
;     return i;
; __device__ __forceinline__ void phase1() { const Ctx c = make_ctx(); PHASE_PTRS;
;     ...
;             if (c.lane == 0) ctl[CW_PROG + j] = (unsigned)n;
.LBB0_293:
	s_waitcnt vmcnt(0)
	v_cmp_eq_u32_e32 vcc, 0, v1
	s_and_saveexec_b64 s[4:5], vcc
	s_cbranch_execz .LBB0_295
	s_ashr_i32 s9, s8, 31
	s_lshl_b64 s[6:7], s[8:9], 2
	s_add_u32 s6, s30, s6
	s_addc_u32 s7, s31, s7
	v_mov_b32_e32 v1, 0x2000
	s_waitcnt vmcnt(0)
	v_mov_b32_e32 v2, s17
	global_store_dword v1, v2, s[6:7]

; __device__ __forceinline__ void t128_load(const float* W, int N, int item, int lane, f32x4 (&v)[16]) {
;     const int nblk = N / 32, kb = item / nblk, nb = item % nblk, k0 = 128 * kb, n0 = 32 * nb;
; #pragma unroll
;     for (int i = 0; i < 16; ++i) v[i] = __builtin_nontemporal_load((const f32x4*)(W + (size_t)(k0 + i * 8 + (lane >> 3)) * N + n0 + (lane & 7) * 4));
; }
; __device__ __forceinline__ void cs_load(int it, int lane, const float* w_gu, const float* w_d, f32x4 (&v)[16]) {
;     if (it < I_D) { constexpr int per = (DFF / 128) * (D / 32); t128_load(w_d + (size_t)(it / per) * DFF * D, D, it % per, lane, v); }
;     else { const int r = it - I_D; constexpr int per = (D / 128) * (4096 / 32); t128_load(w_gu + (size_t)(r / per) * D * 4096, 4096, r % per, lane, v); }
; }
; __device__ __forceinline__ void cs_store(const Ctx& c, int it, const f32x4 (&v)[16], unsigned char* Wgu, unsigned char* Wd) {
;     if (it < I_D) { constexpr int per = (DFF / 128) * (D / 32); t128_store<0>(c, v, DFF, D, Wd + (size_t)(it / per) * D * DFF, it % per); }
;     else { const int r = it - I_D; constexpr int per = (D / 128) * (4096 / 32); t128_store<1>(c, v, D, 4096, Wgu + (size_t)(r / per) * 4096 * D, r % per); }
; }
; __device__ __forceinline__ int conv_stream(const Ctx& c, int j, int first, int step, const unsigned* stop, const float* w_gu, const float* w_d, unsigned char* Wgu, unsigned char* Wd) {
;     int i = first;
;     if (j + CONV_SLOTS * i >= CONV_TOTAL) return i;
;     if (stop && stop_poll(c, stop) >= STOP_AT) return i;
;     f32x4 va[16], vb[16];
;     cs_load(j + CONV_SLOTS * i, c.lane, w_gu, w_d, va);
.LBB0_658:
	v_lshlrev_b32_e32 v2, 2, v1
	v_ashrrev_i32_e32 v59, 31, v58
	v_and_b32_e32 v130, 28, v2
	v_lshlrev_b64 v[2:3], s54, v[58:59]
	v_add_u32_e32 v4, 8, v58
	v_add_u32_e32 v10, 16, v58
	v_add_u32_e32 v12, 24, v58
	v_add_u32_e32 v18, 32, v58
	v_add_u32_e32 v20, 40, v58
	v_add_u32_e32 v26, 48, v58
	v_add_u32_e32 v28, 56, v58
	v_add_u32_e32 v34, 64, v58
	v_add_u32_e32 v36, 0x48, v58
	v_add_u32_e32 v42, 0x50, v58
	v_add_u32_e32 v44, 0x58, v58
	v_add_u32_e32 v50, 0x60, v58
	v_add_u32_e32 v52, 0x68, v58
	v_add_u32_e32 v62, 0x70, v58
	v_add_u32_e32 v58, 0x78, v58
	v_mov_b32_e32 v133, 0
	v_lshlrev_b32_e32 v132, 2, v130
	v_ashrrev_i32_e32 v5, 31, v4
	v_ashrrev_i32_e32 v11, 31, v10
	v_ashrrev_i32_e32 v13, 31, v12
	v_ashrrev_i32_e32 v19, 31, v18
	v_ashrrev_i32_e32 v21, 31, v20
	v_ashrrev_i32_e32 v27, 31, v26
	v_ashrrev_i32_e32 v29, 31, v28
	v_ashrrev_i32_e32 v35, 31, v34
	v_ashrrev_i32_e32 v37, 31, v36
	v_ashrrev_i32_e32 v43, 31, v42
	v_ashrrev_i32_e32 v45, 31, v44
	v_ashrrev_i32_e32 v51, 31, v50
	v_ashrrev_i32_e32 v53, 31, v52
	v_ashrrev_i32_e32 v63, 31, v62
	v_ashrrev_i32_e32 v59, 31, v58
	v_lshl_add_u64 v[60:61], s[56:57], 0, v[132:133]
	v_lshlrev_b64 v[4:5], s54, v[4:5]
	v_lshlrev_b64 v[10:11], s54, v[10:11]
	v_lshlrev_b64 v[12:13], s54, v[12:13]
	v_lshlrev_b64 v[18:19], s54, v[18:19]
	v_lshlrev_b64 v[20:21], s54, v[20:21]
	v_lshlrev_b64 v[26:27], s54, v[26:27]
	v_lshlrev_b64 v[28:29], s54, v[28:29]
	v_lshlrev_b64 v[34:35], s54, v[34:35]
	v_lshlrev_b64 v[36:37], s54, v[36:37]
	v_lshlrev_b64 v[42:43], s54, v[42:43]
	v_lshlrev_b64 v[44:45], s54, v[44:45]
	v_lshlrev_b64 v[50:51], s54, v[50:51]
	v_lshlrev_b64 v[52:53], s54, v[52:53]
	v_lshlrev_b64 v[62:63], s54, v[62:63]
	v_lshlrev_b64 v[58:59], s54, v[58:59]
	v_lshl_add_u64 v[2:3], v[60:61], 0, v[2:3]
	v_lshl_add_u64 v[4:5], v[60:61], 0, v[4:5]
	v_lshl_add_u64 v[10:11], v[60:61], 0, v[10:11]
	v_lshl_add_u64 v[12:13], v[60:61], 0, v[12:13]
	v_lshl_add_u64 v[18:19], v[60:61], 0, v[18:19]
	v_lshl_add_u64 v[20:21], v[60:61], 0, v[20:21]
	v_lshl_add_u64 v[26:27], v[60:61], 0, v[26:27]
	v_lshl_add_u64 v[28:29], v[60:61], 0, v[28:29]
	v_lshl_add_u64 v[34:35], v[60:61], 0, v[34:35]
	v_lshl_add_u64 v[36:37], v[60:61], 0, v[36:37]
	v_lshl_add_u64 v[42:43], v[60:61], 0, v[42:43]
	v_lshl_add_u64 v[44:45], v[60:61], 0, v[44:45]
	v_lshl_add_u64 v[50:51], v[60:61], 0, v[50:51]
	v_lshl_add_u64 v[52:53], v[60:61], 0, v[52:53]
	v_lshl_add_u64 v[62:63], v[60:61], 0, v[62:63]
	v_lshl_add_u64 v[58:59], v[60:61], 0, v[58:59]
	global_load_dwordx4 v[6:9], v[2:3], off nt
	s_nop 0
	global_load_dwordx4 v[2:5], v[4:5], off nt
	s_nop 0
	global_load_dwordx4 v[14:17], v[10:11], off nt
	s_nop 0
	global_load_dwordx4 v[10:13], v[12:13], off nt
	s_nop 0
	global_load_dwordx4 v[22:25], v[18:19], off nt
	s_nop 0
	global_load_dwordx4 v[18:21], v[20:21], off nt
	s_nop 0
	global_load_dwordx4 v[30:33], v[26:27], off nt
	s_nop 0
	global_load_dwordx4 v[26:29], v[28:29], off nt
	s_nop 0
	global_load_dwordx4 v[38:41], v[34:35], off nt
	s_nop 0
	global_load_dwordx4 v[34:37], v[36:37], off nt
	s_nop 0
	global_load_dwordx4 v[46:49], v[42:43], off nt
	s_nop 0
	global_load_dwordx4 v[42:45], v[44:45], off nt
	s_nop 0
	global_load_dwordx4 v[54:57], v[50:51], off nt
	s_nop 0
	global_load_dwordx4 v[50:53], v[52:53], off nt
	s_nop 0
	global_load_dwordx4 v[62:65], v[62:63], off nt
	s_nop 0
	global_load_dwordx4 v[58:61], v[58:59], off nt
	s_add_u32 s14, s34, 0x1e00000
	s_addc_u32 s15, s35, 0
	s_add_u32 s16, s34, 0x21e00000
	s_addc_u32 s17, s35, 0
	s_lshl_b32 s18, s8, 7
	s_lshl_b32 s20, s8, 5
	s_and_b32 s18, s18, 0x3f80
	v_lshlrev_b32_e32 v70, 4, v1
	s_add_u32 s18, s4, s18
	s_mul_i32 s21, s27, 0x4200
	v_and_b32_e32 v134, 0x70, v70
	s_addc_u32 s19, s5, 0
	s_add_i32 s21, s21, 0
	v_mul_u32_u24_e32 v70, 0x84, v134
	v_lshlrev_b32_e32 v71, 2, v131
	v_add_u32_e32 v66, s21, v132
	s_movk_i32 s26, 0x84
	v_add3_u32 v148, s21, v70, v71
	s_lshl_b32 s21, s8, 6
	v_mad_i32_i24 v144, v131, s26, v66
	s_and_b32 s21, s21, 0xf00
	s_lshl_b32 s26, s8, 1
	s_and_b32 s20, s20, 0x60
	s_and_b32 s26, s26, 0x80
	s_or_b32 s20, s20, s21
	v_or_b32_e32 v145, 8, v131
	v_or_b32_e32 v146, 16, v131
	v_or_b32_e32 v147, 24, v131
	s_or_b32 s20, s20, s26
	v_readlane_b32 s21, v252, 14
	v_add_lshl_u32 v136, v131, s20, 11
	v_add_lshl_u32 v138, v145, s20, 11
	v_add_lshl_u32 v140, v146, s20, 11
	v_add_lshl_u32 v142, v147, s20, 11
	s_add_i32 s20, s27, s24
	s_andn2_b32 s21, s21, 63
	s_add_i32 s20, s20, s21
	s_lshl_b32 s21, s25, 3
	v_mul_i32_i24_e32 v67, 0x84, v145
	v_mul_i32_i24_e32 v68, 0x84, v146
	v_mul_i32_i24_e32 v69, 0x84, v147
	s_add_i32 s20, s20, s21
	s_mov_b32 s55, 0
	v_cmp_eq_u32_e64 s[4:5], 0, v1
	v_mov_b32_e32 v135, v133
	v_mov_b32_e32 v137, v133
	v_mov_b32_e32 v139, v133
	v_mov_b32_e32 v141, v133
	v_mov_b32_e32 v143, v133
	s_add_i32 s25, s20, 0x400
	s_add_i32 s24, 0, 0x23e00
	v_add_u32_e32 v149, v66, v67
	v_add_u32_e32 v150, v66, v68
	v_add_u32_e32 v151, v66, v69
	s_waitcnt vmcnt(0)
	s_branch .LBB0_660

; __device__ __forceinline__ void t128_load(const float* W, int N, int item, int lane, f32x4 (&v)[16]) {
;     const int nblk = N / 32, kb = item / nblk, nb = item % nblk, k0 = 128 * kb, n0 = 32 * nb;
; #pragma unroll
;     for (int i = 0; i < 16; ++i) v[i] = __builtin_nontemporal_load((const f32x4*)(W + (size_t)(k0 + i * 8 + (lane >> 3)) * N + n0 + (lane & 7) * 4));
; }
; __device__ __forceinline__ void cs_load(int it, int lane, const float* w_gu, const float* w_d, f32x4 (&v)[16]) {
;     if (it < I_D) { constexpr int per = (DFF / 128) * (D / 32); t128_load(w_d + (size_t)(it / per) * DFF * D, D, it % per, lane, v); }
;     else { const int r = it - I_D; constexpr int per = (D / 128) * (4096 / 32); t128_load(w_gu + (size_t)(r / per) * D * 4096, 4096, r % per, lane, v); }
.LBB0_672:
	s_waitcnt vmcnt(4)
	v_or_b32_e32 v122, s21, v131
	v_ashrrev_i32_e32 v123, 31, v122
	v_lshlrev_b64 v[66:67], s58, v[122:123]
	v_add_u32_e32 v68, 8, v122
	v_add_u32_e32 v74, 16, v122
	v_add_u32_e32 v76, 24, v122
	v_add_u32_e32 v82, 32, v122
	v_add_u32_e32 v84, 40, v122
	v_add_u32_e32 v90, 48, v122
	v_add_u32_e32 v92, 56, v122
	v_add_u32_e32 v98, 64, v122
	v_add_u32_e32 v100, 0x48, v122
	v_add_u32_e32 v106, 0x50, v122
	v_add_u32_e32 v108, 0x58, v122
	v_add_u32_e32 v114, 0x60, v122
	v_add_u32_e32 v116, 0x68, v122
	v_add_u32_e32 v126, 0x70, v122
	v_add_u32_e32 v122, 0x78, v122
	v_lshlrev_b32_e32 v132, 2, v130
	v_ashrrev_i32_e32 v69, 31, v68
	v_ashrrev_i32_e32 v75, 31, v74
	v_ashrrev_i32_e32 v77, 31, v76
	v_ashrrev_i32_e32 v83, 31, v82
	v_ashrrev_i32_e32 v85, 31, v84
	v_ashrrev_i32_e32 v91, 31, v90
	v_ashrrev_i32_e32 v93, 31, v92
	v_ashrrev_i32_e32 v99, 31, v98
	v_ashrrev_i32_e32 v101, 31, v100
	v_ashrrev_i32_e32 v107, 31, v106
	v_ashrrev_i32_e32 v109, 31, v108
	v_ashrrev_i32_e32 v115, 31, v114
	v_ashrrev_i32_e32 v117, 31, v116
	v_ashrrev_i32_e32 v127, 31, v126
	v_ashrrev_i32_e32 v123, 31, v122
	v_lshl_add_u64 v[124:125], s[60:61], 0, v[132:133]
	v_lshlrev_b64 v[68:69], s58, v[68:69]
	v_lshlrev_b64 v[74:75], s58, v[74:75]
	v_lshlrev_b64 v[76:77], s58, v[76:77]
	v_lshlrev_b64 v[82:83], s58, v[82:83]
	v_lshlrev_b64 v[84:85], s58, v[84:85]
	v_lshlrev_b64 v[90:91], s58, v[90:91]
	v_lshlrev_b64 v[92:93], s58, v[92:93]
	v_lshlrev_b64 v[98:99], s58, v[98:99]
	v_lshlrev_b64 v[100:101], s58, v[100:101]
	v_lshlrev_b64 v[106:107], s58, v[106:107]
	v_lshlrev_b64 v[108:109], s58, v[108:109]
	v_lshlrev_b64 v[114:115], s58, v[114:115]
	v_lshlrev_b64 v[116:117], s58, v[116:117]
	v_lshlrev_b64 v[126:127], s58, v[126:127]
	v_lshlrev_b64 v[122:123], s58, v[122:123]
	v_lshl_add_u64 v[66:67], v[124:125], 0, v[66:67]
	v_lshl_add_u64 v[68:69], v[124:125], 0, v[68:69]
	v_lshl_add_u64 v[74:75], v[124:125], 0, v[74:75]
	v_lshl_add_u64 v[76:77], v[124:125], 0, v[76:77]
	v_lshl_add_u64 v[82:83], v[124:125], 0, v[82:83]
	v_lshl_add_u64 v[84:85], v[124:125], 0, v[84:85]
	v_lshl_add_u64 v[90:91], v[124:125], 0, v[90:91]
	v_lshl_add_u64 v[92:93], v[124:125], 0, v[92:93]
	v_lshl_add_u64 v[98:99], v[124:125], 0, v[98:99]
	v_lshl_add_u64 v[100:101], v[124:125], 0, v[100:101]
	v_lshl_add_u64 v[106:107], v[124:125], 0, v[106:107]
	v_lshl_add_u64 v[108:109], v[124:125], 0, v[108:109]
	v_lshl_add_u64 v[114:115], v[124:125], 0, v[114:115]
	v_lshl_add_u64 v[116:117], v[124:125], 0, v[116:117]
	v_lshl_add_u64 v[126:127], v[124:125], 0, v[126:127]
	v_lshl_add_u64 v[122:123], v[124:125], 0, v[122:123]
	global_load_dwordx4 v[70:73], v[66:67], off nt
	s_nop 0
	global_load_dwordx4 v[66:69], v[68:69], off nt
	s_nop 0
	global_load_dwordx4 v[78:81], v[74:75], off nt
	s_nop 0
	global_load_dwordx4 v[74:77], v[76:77], off nt
	s_nop 0
	global_load_dwordx4 v[86:89], v[82:83], off nt
	s_nop 0
	global_load_dwordx4 v[82:85], v[84:85], off nt
	s_nop 0
	global_load_dwordx4 v[94:97], v[90:91], off nt
	s_nop 0
	global_load_dwordx4 v[90:93], v[92:93], off nt
	s_nop 0
	global_load_dwordx4 v[102:105], v[98:99], off nt
	s_nop 0
	global_load_dwordx4 v[98:101], v[100:101], off nt
	s_nop 0
	global_load_dwordx4 v[110:113], v[106:107], off nt
	s_nop 0
	global_load_dwordx4 v[106:109], v[108:109], off nt
	s_nop 0
	global_load_dwordx4 v[118:121], v[114:115], off nt
	s_nop 0
	global_load_dwordx4 v[114:117], v[116:117], off nt
	s_nop 0
	global_load_dwordx4 v[126:129], v[126:127], off nt
	s_nop 0
	global_load_dwordx4 v[122:125], v[122:123], off nt
	s_add_i32 s28, s25, 0xfffff800
	s_mov_b64 s[58:59], -1
	s_cmpk_gt_i32 s28, 0x7fff
	v_add_u32_e32 v154, 0x1080, v144
	v_add_u32_e32 v155, 0x1088, v144
	v_add_u32_e32 v156, 0x14a0, v144
	v_add_u32_e32 v157, 0x14a8, v144
	v_add_u32_e32 v158, 0x18c0, v144
	v_add_u32_e32 v159, 0x18c8, v144
	v_add_u32_e32 v160, 0x1ce0, v144
	v_add_u32_e32 v161, 0x1ce8, v144
	v_add_u32_e32 v162, 0x2100, v144
	v_add_u32_e32 v163, 0x2108, v144
	v_add_u32_e32 v164, 0x2520, v144
	v_add_u32_e32 v165, 0x2528, v144
	v_add_u32_e32 v166, 0x2940, v144
	v_add_u32_e32 v167, 0x2948, v144
	v_add_u32_e32 v168, 0x2d60, v144
	v_add_u32_e32 v169, 0x2d68, v144
	v_add_u32_e32 v170, 0x3180, v144
	v_add_u32_e32 v171, 0x3188, v144
	v_add_u32_e32 v172, 0x35a0, v144
	v_add_u32_e32 v173, 0x35a8, v144
	v_add_u32_e32 v174, 0x39c0, v144
	v_add_u32_e32 v175, 0x39c8, v144
	v_add_u32_e32 v176, 0x3de0, v144
	v_add_u32_e32 v177, 0x3de8, v144
	v_add_u32_e32 v153, 0x400, v148
	v_add_u32_e32 v152, 0x600, v148
	s_cbranch_scc0 .LBB0_691
; #define LAS __attribute__((address_space(3)))
; #define LDS_WAIT() asm volatile("s_waitcnt lgkmcnt(0)" ::: "memory")
; template <int MODE>
; __device__ __forceinline__ void t128_store(const Ctx& c, const f32x4 (&v)[16], int K, int N, unsigned char* WT, int item) {
;     LAS float* scr = (LAS float*)(c.lds + c.wave * CONV_SCR);
;     const int nblk = N / 32, kb = item / nblk, nb = item % nblk, k0 = 128 * kb, n0 = 32 * nb, lane = c.lane;
; #pragma unroll
;     for (int i = 0; i < 16; ++i) { LAS float* d = scr + (i * 8 + (lane >> 3)) * 33 + (lane & 7) * 4; d[0] = v[i].x; d[1] = v[i].y; d[2] = v[i].z; d[3] = v[i].w; }
;     LDS_WAIT(); asm volatile("" ::: "memory");
;     const int cc = lane & 7;
; #pragma unroll
;     for (int j = 0; j < 4; ++j) { const int n = (lane >> 3) + 8 * j; const LAS float* s = scr + (16 * cc) * 33 + n; int w[4];
; #pragma unroll
;         for (int q = 0; q < 4; ++q) { int t = 0; t = __builtin_amdgcn_cvt_pk_fp8_f32(s[(4 * q) * 33] * WSCALE, s[(4 * q + 1) * 33] * WSCALE, t, false);
	s_waitcnt vmcnt(31)
	ds_write2_b32 v144, v6, v7 offset1:1
	ds_write2_b32 v144, v8, v9 offset0:2 offset1:3
	s_waitcnt vmcnt(30)
	ds_write2_b32 v149, v2, v3 offset1:1
	ds_write2_b32 v149, v4, v5 offset0:2 offset1:3
	s_waitcnt vmcnt(29)
	ds_write2_b32 v150, v14, v15 offset1:1
	ds_write2_b32 v150, v16, v17 offset0:2 offset1:3
	s_waitcnt vmcnt(28)
	ds_write2_b32 v151, v10, v11 offset1:1
	ds_write2_b32 v151, v12, v13 offset0:2 offset1:3
	s_waitcnt vmcnt(27)
	ds_write2_b32 v154, v22, v23 offset1:1
	ds_write2_b32 v155, v24, v25 offset1:1
	s_waitcnt vmcnt(26)
	ds_write2_b32 v156, v18, v19 offset1:1
	ds_write2_b32 v157, v20, v21 offset1:1
	s_waitcnt vmcnt(25)
	ds_write2_b32 v158, v30, v31 offset1:1
	ds_write2_b32 v159, v32, v33 offset1:1
	s_waitcnt vmcnt(24)
	ds_write2_b32 v160, v26, v27 offset1:1
	ds_write2_b32 v161, v28, v29 offset1:1
	s_waitcnt vmcnt(23)
	ds_write2_b32 v162, v38, v39 offset1:1
	ds_write2_b32 v163, v40, v41 offset1:1
	s_waitcnt vmcnt(22)
	ds_write2_b32 v164, v34, v35 offset1:1
	ds_write2_b32 v165, v36, v37 offset1:1
	s_waitcnt vmcnt(21)
	ds_write2_b32 v166, v46, v47 offset1:1
	ds_write2_b32 v167, v48, v49 offset1:1
	s_waitcnt vmcnt(20)
	ds_write2_b32 v168, v42, v43 offset1:1
	ds_write2_b32 v169, v44, v45 offset1:1
	s_waitcnt vmcnt(19)
	ds_write2_b32 v170, v54, v55 offset1:1
	ds_write2_b32 v171, v56, v57 offset1:1
	s_waitcnt vmcnt(18)
	ds_write2_b32 v172, v50, v51 offset1:1
	ds_write2_b32 v173, v52, v53 offset1:1
	s_waitcnt vmcnt(17)
	ds_write2_b32 v174, v62, v63 offset1:1
	ds_write2_b32 v175, v64, v65 offset1:1
	s_waitcnt vmcnt(16)
	ds_write2_b32 v176, v58, v59 offset1:1
	ds_write2_b32 v177, v60, v61 offset1:1
	s_waitcnt lgkmcnt(0)
	ds_read2_b32 v[182:183], v148 offset1:8
	ds_read2_b32 v[184:185], v148 offset0:33 offset1:41
	ds_read2_b32 v[188:189], v148 offset0:66 offset1:74
	ds_read2_b32 v[190:191], v148 offset0:99 offset1:107
	v_mov_b32_e32 v178, v133
	ds_read2_b32 v[192:193], v148 offset0:132 offset1:140
	ds_read2_b32 v[194:195], v148 offset0:165 offset1:173
	s_waitcnt lgkmcnt(5)
	v_mul_f32_e32 v179, 0x42800000, v182
	s_waitcnt lgkmcnt(4)
	v_mul_f32_e32 v180, 0x42800000, v184
	v_cvt_pk_fp8_f32 v178, v179, v180
	s_waitcnt lgkmcnt(3)
	v_mul_f32_e32 v179, 0x42800000, v188
	s_waitcnt lgkmcnt(2)
	v_mul_f32_e32 v180, 0x42800000, v190
	ds_read2_b32 v[196:197], v148 offset0:198 offset1:206
	ds_read2_b32 v[198:199], v148 offset0:231 offset1:239
	v_cvt_pk_fp8_f32 v178, v179, v180 op_sel:[0,0,1]
	s_waitcnt lgkmcnt(3)
	v_mul_f32_e32 v180, 0x42800000, v192
	s_waitcnt lgkmcnt(2)
	v_mul_f32_e32 v181, 0x42800000, v194
	v_mov_b32_e32 v179, v133
	ds_read2_b32 v[200:201], v153 offset0:8 offset1:16
	ds_read2_b32 v[202:203], v153 offset0:41 offset1:49
	v_cvt_pk_fp8_f32 v179, v180, v181
	ds_read2_b32 v[204:205], v153 offset0:74 offset1:82
	ds_read2_b32 v[206:207], v153 offset0:107 offset1:115
	ds_read2_b32 v[208:209], v153 offset0:140 offset1:148
	ds_read2_b32 v[210:211], v153 offset0:173 offset1:181
	s_waitcnt lgkmcnt(7)
	v_mul_f32_e32 v180, 0x42800000, v196
	s_waitcnt lgkmcnt(6)
	v_mul_f32_e32 v181, 0x42800000, v198
	v_cvt_pk_fp8_f32 v179, v180, v181 op_sel:[0,0,1]
	s_waitcnt lgkmcnt(5)
	v_mul_f32_e32 v181, 0x42800000, v200
	s_waitcnt lgkmcnt(4)
	v_mul_f32_e32 v182, 0x42800000, v202
	v_mov_b32_e32 v180, v133
	ds_read2_b32 v[212:213], v153 offset0:206 offset1:214
	ds_read2_b32 v[214:215], v153 offset0:239 offset1:247
	v_cvt_pk_fp8_f32 v180, v181, v182
	s_waitcnt lgkmcnt(3)
	v_mul_f32_e32 v188, 0x42800000, v208
	s_waitcnt lgkmcnt(2)
	v_mul_f32_e32 v190, 0x42800000, v210
	v_mov_b32_e32 v181, v133
	v_cvt_pk_fp8_f32 v181, v188, v190
	v_mul_f32_e32 v182, 0x42800000, v204
	v_mul_f32_e32 v184, 0x42800000, v206
	v_cvt_pk_fp8_f32 v180, v182, v184 op_sel:[0,0,1]
	s_waitcnt lgkmcnt(1)
	v_mul_f32_e32 v182, 0x42800000, v212
	s_waitcnt lgkmcnt(0)
; #define LAS __attribute__((address_space(3)))
; #define LDS_WAIT() asm volatile("s_waitcnt lgkmcnt(0)" ::: "memory")
; template <int MODE>
; __device__ __forceinline__ void t128_store(const Ctx& c, const f32x4 (&v)[16], int K, int N, unsigned char* WT, int item) {
;     ...
;     const int cc = lane & 7;
; #pragma unroll
;     for (int j = 0; j < 4; ++j) { const int n = (lane >> 3) + 8 * j; const LAS float* s = scr + (16 * cc) * 33 + n; int w[4];
; #pragma unroll
;         for (int q = 0; q < 4; ++q) { int t = 0; t = __builtin_amdgcn_cvt_pk_fp8_f32(s[(4 * q) * 33] * WSCALE, s[(4 * q + 1) * 33] * WSCALE, t, false);
;             t = __builtin_amdgcn_cvt_pk_fp8_f32(s[(4 * q + 2) * 33] * WSCALE, s[(4 * q + 3) * 33] * WSCALE, t, true); w[q] = t; }
;         const int dr = drow_of<MODE>(n0 + n);
;         __builtin_nontemporal_store((u32x4){(unsigned)w[0], (unsigned)w[1], (unsigned)w[2], (unsigned)w[3]}, (u32x4*)(WT + (size_t)dr * K + k0 + 16 * cc)); }
;     LDS_WAIT(); asm volatile("" ::: "memory");
	v_mul_f32_e32 v184, 0x42800000, v214
	v_cvt_pk_fp8_f32 v181, v182, v184 op_sel:[0,0,1]
	v_mul_f32_e32 v183, 0x42800000, v183
	v_mul_f32_e32 v184, 0x42800000, v185
	v_mov_b32_e32 v182, v133
	v_cvt_pk_fp8_f32 v182, v183, v184
	v_mul_f32_e32 v184, 0x42800000, v189
	v_mul_f32_e32 v188, 0x42800000, v193
	v_mul_f32_e32 v189, 0x42800000, v195
	v_mov_b32_e32 v183, v133
	v_cvt_pk_fp8_f32 v183, v188, v189
	v_mul_f32_e32 v185, 0x42800000, v191
	v_cvt_pk_fp8_f32 v182, v184, v185 op_sel:[0,0,1]
	v_mul_f32_e32 v184, 0x42800000, v197
	v_mul_f32_e32 v185, 0x42800000, v199
	s_add_i32 s20, s25, 0xffff7800
	v_cvt_pk_fp8_f32 v183, v184, v185 op_sel:[0,0,1]
	v_mul_f32_e32 v185, 0x42800000, v201
	v_mul_f32_e32 v188, 0x42800000, v203
	v_mov_b32_e32 v184, v133
	s_lshr_b32 s54, s20, 11
	v_cvt_pk_fp8_f32 v184, v185, v188
	v_mul_f32_e32 v190, 0x42800000, v209
	v_mul_f32_e32 v191, 0x42800000, v211
	v_mov_b32_e32 v185, v133
	s_lshl_b64 s[20:21], s[54:55], 23
	v_cvt_pk_fp8_f32 v185, v190, v191
	s_add_u32 s20, s14, s20
	s_addc_u32 s21, s15, s21
	s_and_b32 s29, s28, 0x780
	v_mul_f32_e32 v188, 0x42800000, v205
	v_mul_f32_e32 v189, 0x42800000, v207
	s_add_u32 s20, s20, s29
	v_cvt_pk_fp8_f32 v184, v188, v189 op_sel:[0,0,1]
	v_mul_f32_e32 v188, 0x42800000, v213
	v_mul_f32_e32 v189, 0x42800000, v215
	s_addc_u32 s21, s21, 0
	v_cvt_pk_fp8_f32 v185, v188, v189 op_sel:[0,0,1]
	v_lshl_add_u64 v[186:187], s[20:21], 0, v[134:135]
	ds_read2_b32 v[188:189], v148 offset0:16 offset1:24
	ds_read2_b32 v[190:191], v148 offset0:49 offset1:57
	v_lshl_add_u64 v[216:217], v[186:187], 0, v[136:137]
	global_store_dwordx4 v[216:217], v[178:181], off nt
	s_nop 1
	v_lshl_add_u64 v[178:179], v[186:187], 0, v[138:139]
	global_store_dwordx4 v[178:179], v[182:185], off nt
	ds_read2_b32 v[182:183], v148 offset0:82 offset1:90
	ds_read2_b32 v[184:185], v148 offset0:115 offset1:123
	s_waitcnt lgkmcnt(3)
	v_mul_f32_e32 v179, 0x42800000, v188
	s_waitcnt lgkmcnt(2)
	v_mul_f32_e32 v180, 0x42800000, v190
	v_mov_b32_e32 v178, v133
	ds_read2_b32 v[192:193], v148 offset0:148 offset1:156
	ds_read2_b32 v[194:195], v148 offset0:181 offset1:189
	v_cvt_pk_fp8_f32 v178, v179, v180
	s_waitcnt lgkmcnt(3)
	v_mul_f32_e32 v179, 0x42800000, v182
	s_waitcnt lgkmcnt(2)
	v_mul_f32_e32 v180, 0x42800000, v184
	ds_read2_b32 v[196:197], v148 offset0:214 offset1:222
	ds_read2_b32 v[198:199], v148 offset0:247 offset1:255
	v_cvt_pk_fp8_f32 v178, v179, v180 op_sel:[0,0,1]
	s_waitcnt lgkmcnt(3)
	v_mul_f32_e32 v180, 0x42800000, v192
	s_waitcnt lgkmcnt(2)
	v_mul_f32_e32 v181, 0x42800000, v194
	v_mov_b32_e32 v179, v133
	ds_read2_b32 v[200:201], v153 offset0:24 offset1:32
	ds_read2_b32 v[202:203], v153 offset0:57 offset1:65
	v_cvt_pk_fp8_f32 v179, v180, v181
	ds_read2_b32 v[204:205], v153 offset0:90 offset1:98
	ds_read2_b32 v[206:207], v153 offset0:123 offset1:131
	ds_read2_b32 v[208:209], v153 offset0:156 offset1:164
	ds_read2_b32 v[210:211], v153 offset0:189 offset1:197
	s_waitcnt lgkmcnt(7)
	v_mul_f32_e32 v180, 0x42800000, v196
	s_waitcnt lgkmcnt(6)
	v_mul_f32_e32 v181, 0x42800000, v198
	v_cvt_pk_fp8_f32 v179, v180, v181 op_sel:[0,0,1]
	s_waitcnt lgkmcnt(5)
	v_mul_f32_e32 v181, 0x42800000, v200
	s_waitcnt lgkmcnt(4)
	v_mul_f32_e32 v182, 0x42800000, v202
	v_mov_b32_e32 v180, v133
	ds_read2_b32 v[212:213], v153 offset0:222 offset1:230
	ds_read2_b32 v[214:215], v152 offset0:127 offset1:135
	v_cvt_pk_fp8_f32 v180, v181, v182
	s_waitcnt lgkmcnt(3)
	v_mul_f32_e32 v188, 0x42800000, v208
	s_waitcnt lgkmcnt(2)
	v_mul_f32_e32 v190, 0x42800000, v210
	v_mov_b32_e32 v181, v133
	v_cvt_pk_fp8_f32 v181, v188, v190
	v_mul_f32_e32 v182, 0x42800000, v204
	v_mul_f32_e32 v184, 0x42800000, v206
	v_cvt_pk_fp8_f32 v180, v182, v184 op_sel:[0,0,1]
	s_waitcnt lgkmcnt(1)
	v_mul_f32_e32 v182, 0x42800000, v212
	s_waitcnt lgkmcnt(0)
	v_mul_f32_e32 v184, 0x42800000, v214
	v_cvt_pk_fp8_f32 v181, v182, v184 op_sel:[0,0,1]
	v_mul_f32_e32 v184, 0x42800000, v189
	v_mul_f32_e32 v188, 0x42800000, v191
	v_mov_b32_e32 v182, v133
	v_cvt_pk_fp8_f32 v182, v184, v188
	v_mul_f32_e32 v184, 0x42800000, v183
	v_mul_f32_e32 v188, 0x42800000, v193
	v_mul_f32_e32 v189, 0x42800000, v195
	v_mov_b32_e32 v183, v133
	v_cvt_pk_fp8_f32 v183, v188, v189
	v_mul_f32_e32 v185, 0x42800000, v185
	v_cvt_pk_fp8_f32 v182, v184, v185 op_sel:[0,0,1]
	v_mul_f32_e32 v184, 0x42800000, v197
	v_mul_f32_e32 v185, 0x42800000, v199
	v_cvt_pk_fp8_f32 v183, v184, v185 op_sel:[0,0,1]
	v_mul_f32_e32 v185, 0x42800000, v201
	v_mul_f32_e32 v188, 0x42800000, v203
	v_mov_b32_e32 v184, v133
	v_cvt_pk_fp8_f32 v184, v185, v188
	v_mul_f32_e32 v190, 0x42800000, v209
	v_mul_f32_e32 v191, 0x42800000, v211
	v_mov_b32_e32 v185, v133
	v_cvt_pk_fp8_f32 v185, v190, v191
	v_mul_f32_e32 v188, 0x42800000, v205
	v_mul_f32_e32 v189, 0x42800000, v207
	v_cvt_pk_fp8_f32 v184, v188, v189 op_sel:[0,0,1]
	v_mul_f32_e32 v188, 0x42800000, v213
	v_mul_f32_e32 v189, 0x42800000, v215
	v_cvt_pk_fp8_f32 v185, v188, v189 op_sel:[0,0,1]
	v_lshl_add_u64 v[188:189], v[186:187], 0, v[140:141]
	global_store_dwordx4 v[188:189], v[178:181], off nt
	s_nop 1
	v_lshl_add_u64 v[178:179], v[186:187], 0, v[142:143]
	global_store_dwordx4 v[178:179], v[182:185], off nt
	s_waitcnt lgkmcnt(0)
	s_cbranch_execz .LBB0_692

; __device__ __forceinline__ void t128_load(const float* W, int N, int item, int lane, f32x4 (&v)[16]) {
;     const int nblk = N / 32, kb = item / nblk, nb = item % nblk, k0 = 128 * kb, n0 = 32 * nb;
; #pragma unroll
;     for (int i = 0; i < 16; ++i) v[i] = __builtin_nontemporal_load((const f32x4*)(W + (size_t)(k0 + i * 8 + (lane >> 3)) * N + n0 + (lane & 7) * 4));
; }
; __device__ __forceinline__ void drain_balanced(const Ctx& c, const unsigned* ctl, const float* w_gu, const float* w_d, unsigned char* Wgu, unsigned char* Wd) {
;     ...
;         int v = lo; int it = __builtin_amdgcn_readfirstlane(item_of(v));
;         f32x4 va[16], vb[16];
;         cs_load(it, c.lane, w_gu, w_d, va);
.LBB0_1191:
	v_lshlrev_b32_e32 v2, 2, v1
	v_and_b32_e32 v130, 28, v2
	v_mov_b32_e32 v133, 0
	v_lshlrev_b32_e32 v132, 2, v130
	v_ashrrev_i32_e32 v59, 31, v58
	v_lshl_add_u64 v[60:61], s[10:11], 0, v[132:133]
	v_lshlrev_b64 v[2:3], s8, v[58:59]
	v_lshl_add_u64 v[10:11], v[60:61], 0, v[2:3]
	v_add_u32_e32 v2, 8, v58
	v_ashrrev_i32_e32 v3, 31, v2
	v_lshlrev_b64 v[2:3], s8, v[2:3]
	v_lshl_add_u64 v[12:13], v[60:61], 0, v[2:3]
	global_load_dwordx4 v[6:9], v[10:11], off nt
	global_load_dwordx4 v[2:5], v[12:13], off nt
	v_add_u32_e32 v10, 16, v58
	v_ashrrev_i32_e32 v11, 31, v10
	v_lshlrev_b64 v[10:11], s8, v[10:11]
	v_lshl_add_u64 v[18:19], v[60:61], 0, v[10:11]
	v_add_u32_e32 v10, 24, v58
	v_ashrrev_i32_e32 v11, 31, v10
	v_lshlrev_b64 v[10:11], s8, v[10:11]
	v_lshl_add_u64 v[20:21], v[60:61], 0, v[10:11]
	global_load_dwordx4 v[14:17], v[18:19], off nt
	global_load_dwordx4 v[10:13], v[20:21], off nt
	v_add_u32_e32 v18, 32, v58
	v_ashrrev_i32_e32 v19, 31, v18
	v_lshlrev_b64 v[18:19], s8, v[18:19]
	v_lshl_add_u64 v[26:27], v[60:61], 0, v[18:19]
	v_add_u32_e32 v18, 40, v58
	v_ashrrev_i32_e32 v19, 31, v18
	v_lshlrev_b64 v[18:19], s8, v[18:19]
	v_lshl_add_u64 v[28:29], v[60:61], 0, v[18:19]
	global_load_dwordx4 v[22:25], v[26:27], off nt
	global_load_dwordx4 v[18:21], v[28:29], off nt
	v_add_u32_e32 v26, 48, v58
	v_ashrrev_i32_e32 v27, 31, v26
	v_lshlrev_b64 v[26:27], s8, v[26:27]
	v_lshl_add_u64 v[34:35], v[60:61], 0, v[26:27]
	v_add_u32_e32 v26, 56, v58
	v_ashrrev_i32_e32 v27, 31, v26
	v_lshlrev_b64 v[26:27], s8, v[26:27]
	v_lshl_add_u64 v[36:37], v[60:61], 0, v[26:27]
	global_load_dwordx4 v[30:33], v[34:35], off nt
	global_load_dwordx4 v[26:29], v[36:37], off nt
	v_add_u32_e32 v34, 64, v58
	v_ashrrev_i32_e32 v35, 31, v34
	v_lshlrev_b64 v[34:35], s8, v[34:35]
	v_lshl_add_u64 v[42:43], v[60:61], 0, v[34:35]
	v_add_u32_e32 v34, 0x48, v58
	v_ashrrev_i32_e32 v35, 31, v34
	v_lshlrev_b64 v[34:35], s8, v[34:35]
	v_lshl_add_u64 v[44:45], v[60:61], 0, v[34:35]
	global_load_dwordx4 v[38:41], v[42:43], off nt
	global_load_dwordx4 v[34:37], v[44:45], off nt
	v_add_u32_e32 v42, 0x50, v58
	v_ashrrev_i32_e32 v43, 31, v42
	v_lshlrev_b64 v[42:43], s8, v[42:43]
	v_lshl_add_u64 v[50:51], v[60:61], 0, v[42:43]
	v_add_u32_e32 v42, 0x58, v58
	v_ashrrev_i32_e32 v43, 31, v42
	v_lshlrev_b64 v[42:43], s8, v[42:43]
	v_lshl_add_u64 v[52:53], v[60:61], 0, v[42:43]
	global_load_dwordx4 v[46:49], v[50:51], off nt
	global_load_dwordx4 v[42:45], v[52:53], off nt
	v_add_u32_e32 v50, 0x60, v58
	v_ashrrev_i32_e32 v51, 31, v50
	v_lshlrev_b64 v[50:51], s8, v[50:51]
	v_lshl_add_u64 v[62:63], v[60:61], 0, v[50:51]
	v_add_u32_e32 v50, 0x68, v58
	v_ashrrev_i32_e32 v51, 31, v50
	v_lshlrev_b64 v[50:51], s8, v[50:51]
	v_lshl_add_u64 v[64:65], v[60:61], 0, v[50:51]
	global_load_dwordx4 v[54:57], v[62:63], off nt
	global_load_dwordx4 v[50:53], v[64:65], off nt
	v_add_u32_e32 v62, 0x70, v58
	v_ashrrev_i32_e32 v63, 31, v62
	v_add_u32_e32 v58, 0x78, v58
	v_lshlrev_b64 v[62:63], s8, v[62:63]
	v_ashrrev_i32_e32 v59, 31, v58
	v_lshl_add_u64 v[66:67], v[60:61], 0, v[62:63]
	v_lshlrev_b64 v[58:59], s8, v[58:59]
	v_lshl_add_u64 v[68:69], v[60:61], 0, v[58:59]
	global_load_dwordx4 v[62:65], v[66:67], off nt
	global_load_dwordx4 v[58:61], v[68:69], off nt
	s_mul_i32 s8, s56, 0x4200
	v_lshlrev_b32_e32 v70, 4, v1
	s_add_i32 s8, s8, 0
	v_or_b32_e32 v137, 8, v131
	v_or_b32_e32 v138, 16, v131
	v_or_b32_e32 v139, 24, v131
	v_and_b32_e32 v134, 0x70, v70
	v_add_u32_e32 v66, s8, v132
	s_movk_i32 s10, 0x84
	v_mul_i32_i24_e32 v67, 0x84, v137
	v_mul_i32_i24_e32 v68, 0x84, v138
	v_mul_i32_i24_e32 v69, 0x84, v139
	v_mul_u32_u24_e32 v70, 0x84, v134
	v_lshlrev_b32_e32 v71, 2, v131
	s_mov_b32 s9, 0
	v_mad_i32_i24 v136, v131, s10, v66
	v_mov_b32_e32 v135, v133
	v_add3_u32 v140, s8, v70, v71
	v_add_u32_e32 v141, v66, v67
	v_add_u32_e32 v142, v66, v68
	v_add_u32_e32 v143, v66, v69
	s_waitcnt vmcnt(0)
	s_branch .LBB0_1193

; __device__ __forceinline__ void t128_load(const float* W, int N, int item, int lane, f32x4 (&v)[16]) {
;     const int nblk = N / 32, kb = item / nblk, nb = item % nblk, k0 = 128 * kb, n0 = 32 * nb;
; #pragma unroll
;     for (int i = 0; i < 16; ++i) v[i] = __builtin_nontemporal_load((const f32x4*)(W + (size_t)(k0 + i * 8 + (lane >> 3)) * N + n0 + (lane & 7) * 4));
; }
; __device__ __forceinline__ void drain_balanced(const Ctx& c, const unsigned* ctl, const float* w_gu, const float* w_d, unsigned char* Wgu, unsigned char* Wd) {
;     ...
;             { const int v2 = v + 1; const bool more = v2 < hi; const int it2 = more ? __builtin_amdgcn_readfirstlane(item_of(v2)) : it;
;               cs_load(it2, c.lane, w_gu, w_d, vb); cs_store(c, it, va, Wgu, Wd); v = v2; it = it2; if (!more) break; }
;             { const int v2 = v + 1; const bool more = v2 < hi; const int it2 = more ? __builtin_amdgcn_readfirstlane(item_of(v2)) : it;
;               cs_load(it2, c.lane, w_gu, w_d, va); cs_store(c, it, vb, Wgu, Wd); v = v2; it = it2; if (!more) break; }
.LBB0_1203:
	s_waitcnt vmcnt(4)
	v_or_b32_e32 v122, s8, v131
	v_lshlrev_b32_e32 v132, 2, v130
	v_ashrrev_i32_e32 v123, 31, v122
	v_lshl_add_u64 v[124:125], s[16:17], 0, v[132:133]
	v_lshlrev_b64 v[66:67], s14, v[122:123]
	v_lshl_add_u64 v[74:75], v[124:125], 0, v[66:67]
	v_add_u32_e32 v66, 8, v122
	v_ashrrev_i32_e32 v67, 31, v66
	v_lshlrev_b64 v[66:67], s14, v[66:67]
	v_lshl_add_u64 v[76:77], v[124:125], 0, v[66:67]
	global_load_dwordx4 v[70:73], v[74:75], off nt
	global_load_dwordx4 v[66:69], v[76:77], off nt
	v_add_u32_e32 v74, 16, v122
	v_ashrrev_i32_e32 v75, 31, v74
	v_lshlrev_b64 v[74:75], s14, v[74:75]
	v_lshl_add_u64 v[82:83], v[124:125], 0, v[74:75]
	v_add_u32_e32 v74, 24, v122
	v_ashrrev_i32_e32 v75, 31, v74
	v_lshlrev_b64 v[74:75], s14, v[74:75]
	v_lshl_add_u64 v[84:85], v[124:125], 0, v[74:75]
	global_load_dwordx4 v[78:81], v[82:83], off nt
	global_load_dwordx4 v[74:77], v[84:85], off nt
	v_add_u32_e32 v82, 32, v122
	v_ashrrev_i32_e32 v83, 31, v82
	v_lshlrev_b64 v[82:83], s14, v[82:83]
	v_lshl_add_u64 v[90:91], v[124:125], 0, v[82:83]
	v_add_u32_e32 v82, 40, v122
	v_ashrrev_i32_e32 v83, 31, v82
	v_lshlrev_b64 v[82:83], s14, v[82:83]
	v_lshl_add_u64 v[92:93], v[124:125], 0, v[82:83]
	global_load_dwordx4 v[86:89], v[90:91], off nt
	global_load_dwordx4 v[82:85], v[92:93], off nt
	v_add_u32_e32 v90, 48, v122
	v_ashrrev_i32_e32 v91, 31, v90
	v_lshlrev_b64 v[90:91], s14, v[90:91]
	v_lshl_add_u64 v[98:99], v[124:125], 0, v[90:91]
	v_add_u32_e32 v90, 56, v122
	v_ashrrev_i32_e32 v91, 31, v90
	v_lshlrev_b64 v[90:91], s14, v[90:91]
	v_lshl_add_u64 v[100:101], v[124:125], 0, v[90:91]
	global_load_dwordx4 v[94:97], v[98:99], off nt
	global_load_dwordx4 v[90:93], v[100:101], off nt
	v_add_u32_e32 v98, 64, v122
	v_add_u32_e32 v100, 0x48, v122
	v_add_u32_e32 v106, 0x50, v122
	v_add_u32_e32 v108, 0x58, v122
	v_add_u32_e32 v114, 0x60, v122
	v_add_u32_e32 v116, 0x68, v122
	v_add_u32_e32 v126, 0x70, v122
	v_add_u32_e32 v122, 0x78, v122
	v_ashrrev_i32_e32 v99, 31, v98
	v_ashrrev_i32_e32 v101, 31, v100
	v_ashrrev_i32_e32 v107, 31, v106
	v_ashrrev_i32_e32 v109, 31, v108
	v_ashrrev_i32_e32 v115, 31, v114
	v_ashrrev_i32_e32 v117, 31, v116
	v_ashrrev_i32_e32 v127, 31, v126
	v_ashrrev_i32_e32 v123, 31, v122
	v_lshlrev_b64 v[98:99], s14, v[98:99]
	v_lshlrev_b64 v[100:101], s14, v[100:101]
	v_lshlrev_b64 v[106:107], s14, v[106:107]
	v_lshlrev_b64 v[108:109], s14, v[108:109]
	v_lshlrev_b64 v[114:115], s14, v[114:115]
	v_lshlrev_b64 v[116:117], s14, v[116:117]
	v_lshlrev_b64 v[126:127], s14, v[126:127]
	v_lshlrev_b64 v[122:123], s14, v[122:123]
	v_lshl_add_u64 v[98:99], v[124:125], 0, v[98:99]
	v_lshl_add_u64 v[100:101], v[124:125], 0, v[100:101]
	v_lshl_add_u64 v[106:107], v[124:125], 0, v[106:107]
	v_lshl_add_u64 v[108:109], v[124:125], 0, v[108:109]
	v_lshl_add_u64 v[114:115], v[124:125], 0, v[114:115]
	v_lshl_add_u64 v[116:117], v[124:125], 0, v[116:117]
	v_lshl_add_u64 v[126:127], v[124:125], 0, v[126:127]
	v_lshl_add_u64 v[122:123], v[124:125], 0, v[122:123]
	global_load_dwordx4 v[102:105], v[98:99], off nt
	s_nop 0
	global_load_dwordx4 v[98:101], v[100:101], off nt
	s_nop 0
	global_load_dwordx4 v[110:113], v[106:107], off nt
	s_nop 0
	global_load_dwordx4 v[106:109], v[108:109], off nt
	s_nop 0
	global_load_dwordx4 v[118:121], v[114:115], off nt
	s_nop 0
	global_load_dwordx4 v[114:117], v[116:117], off nt
	s_nop 0
	global_load_dwordx4 v[126:129], v[126:127], off nt
	s_nop 0
	global_load_dwordx4 v[122:125], v[122:123], off nt
	s_mov_b64 s[14:15], -1
	s_cmpk_gt_i32 s24, 0x7fff
	v_add_u32_e32 v146, 0x1080, v136
	v_add_u32_e32 v147, 0x1088, v136
	v_add_u32_e32 v148, 0x14a0, v136
	v_add_u32_e32 v149, 0x14a8, v136
	v_add_u32_e32 v150, 0x18c0, v136
	v_add_u32_e32 v151, 0x18c8, v136
	v_add_u32_e32 v152, 0x1ce0, v136
	v_add_u32_e32 v153, 0x1ce8, v136
	v_add_u32_e32 v154, 0x2100, v136
	v_add_u32_e32 v155, 0x2108, v136
	v_add_u32_e32 v156, 0x2520, v136
	v_add_u32_e32 v157, 0x2528, v136
	v_add_u32_e32 v158, 0x2940, v136
	v_add_u32_e32 v159, 0x2948, v136
	v_add_u32_e32 v160, 0x2d60, v136
	v_add_u32_e32 v161, 0x2d68, v136
	v_add_u32_e32 v163, 0x3180, v136
	v_add_u32_e32 v164, 0x3188, v136
	v_add_u32_e32 v165, 0x35a0, v136
	v_add_u32_e32 v166, 0x35a8, v136
	v_add_u32_e32 v167, 0x39c0, v136
	v_add_u32_e32 v168, 0x39c8, v136
	v_add_u32_e32 v169, 0x3de0, v136
	v_add_u32_e32 v170, 0x3de8, v136
	v_add_u32_e32 v145, 0x400, v140
	v_add_u32_e32 v144, 0x600, v140
	s_cbranch_scc0 .LBB0_1205
; #define LAS __attribute__((address_space(3)))
; #define LDS_WAIT() asm volatile("s_waitcnt lgkmcnt(0)" ::: "memory")
; template <int MODE>
; __device__ __forceinline__ void t128_store(const Ctx& c, const f32x4 (&v)[16], int K, int N, unsigned char* WT, int item) {
;     LAS float* scr = (LAS float*)(c.lds + c.wave * CONV_SCR);
;     const int nblk = N / 32, kb = item / nblk, nb = item % nblk, k0 = 128 * kb, n0 = 32 * nb, lane = c.lane;
; #pragma unroll
;     for (int i = 0; i < 16; ++i) { LAS float* d = scr + (i * 8 + (lane >> 3)) * 33 + (lane & 7) * 4; d[0] = v[i].x; d[1] = v[i].y; d[2] = v[i].z; d[3] = v[i].w; }
;     LDS_WAIT(); asm volatile("" ::: "memory");
;     const int cc = lane & 7;
; #pragma unroll
;     for (int j = 0; j < 4; ++j) { const int n = (lane >> 3) + 8 * j; const LAS float* s = scr + (16 * cc) * 33 + n; int w[4];
; #pragma unroll
;         for (int q = 0; q < 4; ++q) { int t = 0; t = __builtin_amdgcn_cvt_pk_fp8_f32(s[(4 * q) * 33] * WSCALE, s[(4 * q + 1) * 33] * WSCALE, t, false);
	s_waitcnt vmcnt(31)
	ds_write2_b32 v136, v6, v7 offset1:1
	ds_write2_b32 v136, v8, v9 offset0:2 offset1:3
	s_waitcnt vmcnt(30)
	ds_write2_b32 v141, v2, v3 offset1:1
	ds_write2_b32 v141, v4, v5 offset0:2 offset1:3
	s_waitcnt vmcnt(29)
	ds_write2_b32 v142, v14, v15 offset1:1
	ds_write2_b32 v142, v16, v17 offset0:2 offset1:3
	s_waitcnt vmcnt(28)
	ds_write2_b32 v143, v10, v11 offset1:1
	ds_write2_b32 v143, v12, v13 offset0:2 offset1:3
	s_waitcnt vmcnt(27)
	ds_write2_b32 v146, v22, v23 offset1:1
	ds_write2_b32 v147, v24, v25 offset1:1
	s_waitcnt vmcnt(26)
	ds_write2_b32 v148, v18, v19 offset1:1
	ds_write2_b32 v149, v20, v21 offset1:1
	s_waitcnt vmcnt(25)
	ds_write2_b32 v150, v30, v31 offset1:1
	ds_write2_b32 v151, v32, v33 offset1:1
	s_waitcnt vmcnt(24)
	ds_write2_b32 v152, v26, v27 offset1:1
	ds_write2_b32 v153, v28, v29 offset1:1
	s_waitcnt vmcnt(23)
	ds_write2_b32 v154, v38, v39 offset1:1
	ds_write2_b32 v155, v40, v41 offset1:1
	s_waitcnt vmcnt(22)
	ds_write2_b32 v156, v34, v35 offset1:1
	ds_write2_b32 v157, v36, v37 offset1:1
	s_waitcnt vmcnt(21)
	ds_write2_b32 v158, v46, v47 offset1:1
	ds_write2_b32 v159, v48, v49 offset1:1
	s_waitcnt vmcnt(20)
	ds_write2_b32 v160, v42, v43 offset1:1
	ds_write2_b32 v161, v44, v45 offset1:1
	s_waitcnt vmcnt(19)
	ds_write2_b32 v163, v54, v55 offset1:1
	ds_write2_b32 v164, v56, v57 offset1:1
	s_waitcnt vmcnt(18)
	ds_write2_b32 v165, v50, v51 offset1:1
	ds_write2_b32 v166, v52, v53 offset1:1
	s_waitcnt vmcnt(17)
	ds_write2_b32 v167, v62, v63 offset1:1
	ds_write2_b32 v168, v64, v65 offset1:1
	s_waitcnt vmcnt(16)
	ds_write2_b32 v169, v58, v59 offset1:1
	ds_write2_b32 v170, v60, v61 offset1:1
	s_waitcnt lgkmcnt(0)
	ds_read2_b32 v[176:177], v140 offset1:8
	ds_read2_b32 v[178:179], v140 offset0:33 offset1:41
	ds_read2_b32 v[182:183], v140 offset0:66 offset1:74
	ds_read2_b32 v[184:185], v140 offset0:99 offset1:107
	v_mov_b32_e32 v172, v133
	ds_read2_b32 v[186:187], v140 offset0:132 offset1:140
	ds_read2_b32 v[188:189], v140 offset0:165 offset1:173
	s_waitcnt lgkmcnt(5)
	v_mul_f32_e32 v171, 0x42800000, v176
	s_waitcnt lgkmcnt(4)
	v_mul_f32_e32 v173, 0x42800000, v178
	v_cvt_pk_fp8_f32 v172, v171, v173
	s_waitcnt lgkmcnt(3)
	v_mul_f32_e32 v171, 0x42800000, v182
	s_waitcnt lgkmcnt(2)
	v_mul_f32_e32 v173, 0x42800000, v184
	ds_read2_b32 v[190:191], v140 offset0:198 offset1:206
	ds_read2_b32 v[192:193], v140 offset0:231 offset1:239
	v_cvt_pk_fp8_f32 v172, v171, v173 op_sel:[0,0,1]
	s_waitcnt lgkmcnt(3)
	v_mul_f32_e32 v171, 0x42800000, v186
	s_waitcnt lgkmcnt(2)
	v_mul_f32_e32 v174, 0x42800000, v188
	v_mov_b32_e32 v173, v133
	ds_read2_b32 v[194:195], v145 offset0:8 offset1:16
	ds_read2_b32 v[196:197], v145 offset0:41 offset1:49
	v_cvt_pk_fp8_f32 v173, v171, v174
	ds_read2_b32 v[198:199], v145 offset0:74 offset1:82
	ds_read2_b32 v[200:201], v145 offset0:107 offset1:115
	ds_read2_b32 v[202:203], v145 offset0:140 offset1:148
	ds_read2_b32 v[204:205], v145 offset0:173 offset1:181
	s_add_i32 s8, s24, 0xffff8000
	s_lshr_b32 s8, s8, 11
	s_waitcnt lgkmcnt(7)
	v_mul_f32_e32 v171, 0x42800000, v190
	s_waitcnt lgkmcnt(6)
	v_mul_f32_e32 v174, 0x42800000, v192
	s_lshl_b64 s[14:15], s[8:9], 23
	v_cvt_pk_fp8_f32 v173, v171, v174 op_sel:[0,0,1]
	s_waitcnt lgkmcnt(5)
	v_mul_f32_e32 v171, 0x42800000, v194
	s_waitcnt lgkmcnt(4)
	v_mul_f32_e32 v175, 0x42800000, v196
	v_mov_b32_e32 v174, v133
	ds_read2_b32 v[206:207], v145 offset0:206 offset1:214
	ds_read2_b32 v[208:209], v145 offset0:239 offset1:247
	s_add_u32 s8, s52, s14
	v_cvt_pk_fp8_f32 v174, v171, v175
	s_waitcnt lgkmcnt(3)
	v_mul_f32_e32 v178, 0x42800000, v202
	s_waitcnt lgkmcnt(2)
	v_mul_f32_e32 v182, 0x42800000, v204
	v_mov_b32_e32 v175, v133
	s_addc_u32 s15, s53, s15
	s_lshl_b32 s16, s24, 5
	s_and_b32 s14, s24, 0x780
	v_cvt_pk_fp8_f32 v175, v178, v182
	s_add_u32 s14, s8, s14
	s_addc_u32 s15, s15, 0
	v_mul_f32_e32 v171, 0x42800000, v198
	v_mul_f32_e32 v176, 0x42800000, v200
	s_lshl_b32 s8, s24, 6
	v_lshl_add_u64 v[180:181], s[14:15], 0, v[134:135]
	v_cvt_pk_fp8_f32 v174, v171, v176 op_sel:[0,0,1]
	s_waitcnt lgkmcnt(1)
	v_mul_f32_e32 v171, 0x42800000, v206
	s_waitcnt lgkmcnt(0)
; #define LAS __attribute__((address_space(3)))
; #define LDS_WAIT() asm volatile("s_waitcnt lgkmcnt(0)" ::: "memory")
; template <int MODE>
; __device__ __forceinline__ void t128_store(const Ctx& c, const f32x4 (&v)[16], int K, int N, unsigned char* WT, int item) {
;     ...
;     const int cc = lane & 7;
; #pragma unroll
;     for (int j = 0; j < 4; ++j) { const int n = (lane >> 3) + 8 * j; const LAS float* s = scr + (16 * cc) * 33 + n; int w[4];
; #pragma unroll
;         for (int q = 0; q < 4; ++q) { int t = 0; t = __builtin_amdgcn_cvt_pk_fp8_f32(s[(4 * q) * 33] * WSCALE, s[(4 * q + 1) * 33] * WSCALE, t, false);
;             t = __builtin_amdgcn_cvt_pk_fp8_f32(s[(4 * q + 2) * 33] * WSCALE, s[(4 * q + 3) * 33] * WSCALE, t, true); w[q] = t; }
;         const int dr = drow_of<MODE>(n0 + n);
;         __builtin_nontemporal_store((u32x4){(unsigned)w[0], (unsigned)w[1], (unsigned)w[2], (unsigned)w[3]}, (u32x4*)(WT + (size_t)dr * K + k0 + 16 * cc)); }
;     LDS_WAIT(); asm volatile("" ::: "memory");
	v_mul_f32_e32 v176, 0x42800000, v208
	s_and_b32 s8, s8, 0xf00
	s_lshl_b32 s14, s24, 1
	s_and_b32 s15, s16, 0x60
	v_cvt_pk_fp8_f32 v175, v171, v176 op_sel:[0,0,1]
	s_and_b32 s14, s14, 0x80
	s_or_b32 s8, s15, s8
	s_or_b32 s8, s8, s14
	v_add_lshl_u32 v210, s8, v131, 11
	v_mov_b32_e32 v211, v133
	v_lshl_add_u64 v[210:211], v[180:181], 0, v[210:211]
	global_store_dwordx4 v[210:211], v[172:175], off nt
	v_mul_f32_e32 v171, 0x42800000, v177
	v_mul_f32_e32 v176, 0x42800000, v189
	v_mul_f32_e32 v173, 0x42800000, v179
	v_mov_b32_e32 v172, v133
	v_cvt_pk_fp8_f32 v172, v171, v173
	v_mul_f32_e32 v175, 0x42800000, v187
	v_mov_b32_e32 v173, v133
	v_cvt_pk_fp8_f32 v173, v175, v176
	v_mul_f32_e32 v171, 0x42800000, v183
	v_mul_f32_e32 v174, 0x42800000, v185
	v_cvt_pk_fp8_f32 v172, v171, v174 op_sel:[0,0,1]
	v_mul_f32_e32 v171, 0x42800000, v191
	v_mul_f32_e32 v174, 0x42800000, v193
	v_cvt_pk_fp8_f32 v173, v171, v174 op_sel:[0,0,1]
	v_mul_f32_e32 v171, 0x42800000, v195
	v_mul_f32_e32 v175, 0x42800000, v197
	v_mov_b32_e32 v174, v133
	v_cvt_pk_fp8_f32 v174, v171, v175
	v_mul_f32_e32 v177, 0x42800000, v203
	v_mul_f32_e32 v178, 0x42800000, v205
	v_mov_b32_e32 v175, v133
	v_cvt_pk_fp8_f32 v175, v177, v178
	v_mul_f32_e32 v171, 0x42800000, v199
	v_mul_f32_e32 v176, 0x42800000, v201
	v_cvt_pk_fp8_f32 v174, v171, v176 op_sel:[0,0,1]
	v_mul_f32_e32 v171, 0x42800000, v207
	v_mul_f32_e32 v176, 0x42800000, v209
	v_cvt_pk_fp8_f32 v175, v171, v176 op_sel:[0,0,1]
	ds_read2_b32 v[178:179], v140 offset0:16 offset1:24
	ds_read2_b32 v[182:183], v140 offset0:49 offset1:57
	v_add_lshl_u32 v176, s8, v137, 11
	v_mov_b32_e32 v177, v133
	v_lshl_add_u64 v[176:177], v[180:181], 0, v[176:177]
	global_store_dwordx4 v[176:177], v[172:175], off nt
	ds_read2_b32 v[176:177], v140 offset0:82 offset1:90
	ds_read2_b32 v[184:185], v140 offset0:115 offset1:123
	s_waitcnt lgkmcnt(3)
	v_mul_f32_e32 v171, 0x42800000, v178
	s_waitcnt lgkmcnt(2)
	v_mul_f32_e32 v173, 0x42800000, v182
	v_mov_b32_e32 v172, v133
	ds_read2_b32 v[186:187], v140 offset0:148 offset1:156
	ds_read2_b32 v[188:189], v140 offset0:181 offset1:189
	v_cvt_pk_fp8_f32 v172, v171, v173
	s_waitcnt lgkmcnt(3)
	v_mul_f32_e32 v171, 0x42800000, v176
	s_waitcnt lgkmcnt(2)
	v_mul_f32_e32 v173, 0x42800000, v184
	ds_read2_b32 v[190:191], v140 offset0:214 offset1:222
	ds_read2_b32 v[192:193], v140 offset0:247 offset1:255
	v_cvt_pk_fp8_f32 v172, v171, v173 op_sel:[0,0,1]
	s_waitcnt lgkmcnt(3)
	v_mul_f32_e32 v171, 0x42800000, v186
	s_waitcnt lgkmcnt(2)
	v_mul_f32_e32 v174, 0x42800000, v188
	v_mov_b32_e32 v173, v133
	ds_read2_b32 v[194:195], v145 offset0:24 offset1:32
	ds_read2_b32 v[196:197], v145 offset0:57 offset1:65
	v_cvt_pk_fp8_f32 v173, v171, v174
	ds_read2_b32 v[198:199], v145 offset0:90 offset1:98
	ds_read2_b32 v[200:201], v145 offset0:123 offset1:131
	ds_read2_b32 v[202:203], v145 offset0:156 offset1:164
	ds_read2_b32 v[204:205], v145 offset0:189 offset1:197
	s_waitcnt lgkmcnt(7)
	v_mul_f32_e32 v171, 0x42800000, v190
	s_waitcnt lgkmcnt(6)
	v_mul_f32_e32 v174, 0x42800000, v192
	v_cvt_pk_fp8_f32 v173, v171, v174 op_sel:[0,0,1]
	s_waitcnt lgkmcnt(5)
	v_mul_f32_e32 v171, 0x42800000, v194
	s_waitcnt lgkmcnt(4)
	v_mul_f32_e32 v175, 0x42800000, v196
	v_mov_b32_e32 v174, v133
	ds_read2_b32 v[206:207], v145 offset0:222 offset1:230
	ds_read2_b32 v[208:209], v144 offset0:127 offset1:135
	v_cvt_pk_fp8_f32 v174, v171, v175
	s_waitcnt lgkmcnt(3)
	v_mul_f32_e32 v178, 0x42800000, v202
	s_waitcnt lgkmcnt(2)
	v_mul_f32_e32 v182, 0x42800000, v204
	v_mov_b32_e32 v175, v133
	v_cvt_pk_fp8_f32 v175, v178, v182
	v_mul_f32_e32 v171, 0x42800000, v198
	v_mul_f32_e32 v176, 0x42800000, v200
	v_cvt_pk_fp8_f32 v174, v171, v176 op_sel:[0,0,1]
	s_waitcnt lgkmcnt(1)
	v_mul_f32_e32 v171, 0x42800000, v206
	s_waitcnt lgkmcnt(0)
	v_mul_f32_e32 v176, 0x42800000, v208
	v_cvt_pk_fp8_f32 v175, v171, v176 op_sel:[0,0,1]
	v_add_lshl_u32 v210, s8, v138, 11
	v_mov_b32_e32 v211, v133
	v_lshl_add_u64 v[210:211], v[180:181], 0, v[210:211]
	global_store_dwordx4 v[210:211], v[172:175], off nt
	v_mul_f32_e32 v171, 0x42800000, v179
	v_mul_f32_e32 v176, 0x42800000, v189
	v_mul_f32_e32 v173, 0x42800000, v183
	v_mov_b32_e32 v172, v133
	v_cvt_pk_fp8_f32 v172, v171, v173
	v_mul_f32_e32 v175, 0x42800000, v187
	v_mov_b32_e32 v173, v133
	v_cvt_pk_fp8_f32 v173, v175, v176
	v_mul_f32_e32 v171, 0x42800000, v177
	v_mul_f32_e32 v174, 0x42800000, v185
	v_cvt_pk_fp8_f32 v172, v171, v174 op_sel:[0,0,1]
	v_mul_f32_e32 v171, 0x42800000, v191
	v_mul_f32_e32 v174, 0x42800000, v193
	v_cvt_pk_fp8_f32 v173, v171, v174 op_sel:[0,0,1]
	v_mul_f32_e32 v171, 0x42800000, v195
	v_mul_f32_e32 v175, 0x42800000, v197
	v_mov_b32_e32 v174, v133
	v_cvt_pk_fp8_f32 v174, v171, v175
	v_mul_f32_e32 v177, 0x42800000, v203
	v_mul_f32_e32 v178, 0x42800000, v205
	v_mov_b32_e32 v175, v133
	v_cvt_pk_fp8_f32 v175, v177, v178
	v_mul_f32_e32 v171, 0x42800000, v199
	v_mul_f32_e32 v176, 0x42800000, v201
	v_cvt_pk_fp8_f32 v174, v171, v176 op_sel:[0,0,1]
	v_mul_f32_e32 v171, 0x42800000, v207
	v_mul_f32_e32 v176, 0x42800000, v209
	v_cvt_pk_fp8_f32 v175, v171, v176 op_sel:[0,0,1]
	v_add_lshl_u32 v176, s8, v139, 11
	v_mov_b32_e32 v177, v133
	v_lshl_add_u64 v[176:177], v[180:181], 0, v[176:177]
	global_store_dwordx4 v[176:177], v[172:175], off nt
	s_waitcnt lgkmcnt(0)
	s_cbranch_execnz .LBB0_1207
	s_branch .LBB0_1206

; __device__ __forceinline__ void t128_load(const float* W, int N, int item, int lane, f32x4 (&v)[16]) {
;     const int nblk = N / 32, kb = item / nblk, nb = item % nblk, k0 = 128 * kb, n0 = 32 * nb;
; #pragma unroll
;     for (int i = 0; i < 16; ++i) v[i] = __builtin_nontemporal_load((const f32x4*)(W + (size_t)(k0 + i * 8 + (lane >> 3)) * N + n0 + (lane & 7) * 4));
; }
; __device__ __forceinline__ void drain_balanced(const Ctx& c, const unsigned* ctl, const float* w_gu, const float* w_d, unsigned char* Wgu, unsigned char* Wd) {
;     ...
;         int v = lo; int it = __builtin_amdgcn_readfirstlane(item_of(v));
;         f32x4 va[16], vb[16];
;         cs_load(it, c.lane, w_gu, w_d, va);
.LBB0_1332:
	v_lshlrev_b32_e32 v2, 2, v1
	v_and_b32_e32 v130, 28, v2
	v_mov_b32_e32 v133, 0
	v_lshlrev_b32_e32 v132, 2, v130
	v_ashrrev_i32_e32 v59, 31, v58
	v_lshl_add_u64 v[60:61], s[10:11], 0, v[132:133]
	v_lshlrev_b64 v[2:3], s8, v[58:59]
	v_lshl_add_u64 v[10:11], v[60:61], 0, v[2:3]
	v_add_u32_e32 v2, 8, v58
	v_ashrrev_i32_e32 v3, 31, v2
	v_lshlrev_b64 v[2:3], s8, v[2:3]
	v_lshl_add_u64 v[12:13], v[60:61], 0, v[2:3]
	global_load_dwordx4 v[6:9], v[10:11], off nt
	global_load_dwordx4 v[2:5], v[12:13], off nt
	v_add_u32_e32 v10, 16, v58
	v_ashrrev_i32_e32 v11, 31, v10
	v_lshlrev_b64 v[10:11], s8, v[10:11]
	v_lshl_add_u64 v[18:19], v[60:61], 0, v[10:11]
	v_add_u32_e32 v10, 24, v58
	v_ashrrev_i32_e32 v11, 31, v10
	v_lshlrev_b64 v[10:11], s8, v[10:11]
	v_lshl_add_u64 v[20:21], v[60:61], 0, v[10:11]
	global_load_dwordx4 v[14:17], v[18:19], off nt
	global_load_dwordx4 v[10:13], v[20:21], off nt
	v_add_u32_e32 v18, 32, v58
	v_ashrrev_i32_e32 v19, 31, v18
	v_lshlrev_b64 v[18:19], s8, v[18:19]
	v_lshl_add_u64 v[26:27], v[60:61], 0, v[18:19]
	v_add_u32_e32 v18, 40, v58
	v_ashrrev_i32_e32 v19, 31, v18
	v_lshlrev_b64 v[18:19], s8, v[18:19]
	v_lshl_add_u64 v[28:29], v[60:61], 0, v[18:19]
	global_load_dwordx4 v[22:25], v[26:27], off nt
	global_load_dwordx4 v[18:21], v[28:29], off nt
	v_add_u32_e32 v26, 48, v58
	v_ashrrev_i32_e32 v27, 31, v26
	v_lshlrev_b64 v[26:27], s8, v[26:27]
	v_lshl_add_u64 v[34:35], v[60:61], 0, v[26:27]
	v_add_u32_e32 v26, 56, v58
	v_ashrrev_i32_e32 v27, 31, v26
	v_lshlrev_b64 v[26:27], s8, v[26:27]
	v_lshl_add_u64 v[36:37], v[60:61], 0, v[26:27]
	global_load_dwordx4 v[30:33], v[34:35], off nt
	global_load_dwordx4 v[26:29], v[36:37], off nt
	v_add_u32_e32 v34, 64, v58
	v_ashrrev_i32_e32 v35, 31, v34
	v_lshlrev_b64 v[34:35], s8, v[34:35]
	v_lshl_add_u64 v[42:43], v[60:61], 0, v[34:35]
	v_add_u32_e32 v34, 0x48, v58
	v_ashrrev_i32_e32 v35, 31, v34
	v_lshlrev_b64 v[34:35], s8, v[34:35]
	v_lshl_add_u64 v[44:45], v[60:61], 0, v[34:35]
	global_load_dwordx4 v[38:41], v[42:43], off nt
	global_load_dwordx4 v[34:37], v[44:45], off nt
	v_add_u32_e32 v42, 0x50, v58
	v_ashrrev_i32_e32 v43, 31, v42
	v_lshlrev_b64 v[42:43], s8, v[42:43]
	v_lshl_add_u64 v[50:51], v[60:61], 0, v[42:43]
	v_add_u32_e32 v42, 0x58, v58
	v_ashrrev_i32_e32 v43, 31, v42
	v_lshlrev_b64 v[42:43], s8, v[42:43]
	v_lshl_add_u64 v[52:53], v[60:61], 0, v[42:43]
	global_load_dwordx4 v[46:49], v[50:51], off nt
	global_load_dwordx4 v[42:45], v[52:53], off nt
	v_add_u32_e32 v50, 0x60, v58
	v_ashrrev_i32_e32 v51, 31, v50
	v_lshlrev_b64 v[50:51], s8, v[50:51]
	v_lshl_add_u64 v[62:63], v[60:61], 0, v[50:51]
	v_add_u32_e32 v50, 0x68, v58
	v_ashrrev_i32_e32 v51, 31, v50
	v_lshlrev_b64 v[50:51], s8, v[50:51]
	v_lshl_add_u64 v[64:65], v[60:61], 0, v[50:51]
	global_load_dwordx4 v[54:57], v[62:63], off nt
	global_load_dwordx4 v[50:53], v[64:65], off nt
	v_add_u32_e32 v62, 0x70, v58
	v_ashrrev_i32_e32 v63, 31, v62
	v_add_u32_e32 v58, 0x78, v58
	v_lshlrev_b64 v[62:63], s8, v[62:63]
	v_ashrrev_i32_e32 v59, 31, v58
	v_lshl_add_u64 v[66:67], v[60:61], 0, v[62:63]
	v_lshlrev_b64 v[58:59], s8, v[58:59]
	v_lshl_add_u64 v[68:69], v[60:61], 0, v[58:59]
	global_load_dwordx4 v[62:65], v[66:67], off nt
	global_load_dwordx4 v[58:61], v[68:69], off nt
	s_mulk_i32 s56, 0x4200
	v_lshlrev_b32_e32 v1, 4, v1
	s_add_i32 s8, s56, 0
	v_or_b32_e32 v137, 8, v131
	v_or_b32_e32 v138, 16, v131
	v_or_b32_e32 v139, 24, v131
	v_and_b32_e32 v134, 0x70, v1
	v_add_u32_e32 v66, s8, v132
	s_movk_i32 s10, 0x84
	v_mul_i32_i24_e32 v67, 0x84, v137
	v_mul_i32_i24_e32 v68, 0x84, v138
	v_mul_i32_i24_e32 v69, 0x84, v139
	v_mul_u32_u24_e32 v1, 0x84, v134
	v_lshlrev_b32_e32 v70, 2, v131
	s_mov_b32 s9, 0
	v_mad_i32_i24 v136, v131, s10, v66
	v_mov_b32_e32 v135, v133
	v_add3_u32 v1, s8, v1, v70
	v_add_u32_e32 v140, v66, v67
	v_add_u32_e32 v141, v66, v68
	v_add_u32_e32 v142, v66, v69
	s_waitcnt vmcnt(0)
	s_branch .LBB0_1334

; __device__ __forceinline__ void t128_load(const float* W, int N, int item, int lane, f32x4 (&v)[16]) {
;     const int nblk = N / 32, kb = item / nblk, nb = item % nblk, k0 = 128 * kb, n0 = 32 * nb;
; #pragma unroll
;     for (int i = 0; i < 16; ++i) v[i] = __builtin_nontemporal_load((const f32x4*)(W + (size_t)(k0 + i * 8 + (lane >> 3)) * N + n0 + (lane & 7) * 4));
; }
; __device__ __forceinline__ void cs_load(int it, int lane, const float* w_gu, const float* w_d, f32x4 (&v)[16]) {
;     if (it < I_D) { constexpr int per = (DFF / 128) * (D / 32); t128_load(w_d + (size_t)(it / per) * DFF * D, D, it % per, lane, v); }
;     else { const int r = it - I_D; constexpr int per = (D / 128) * (4096 / 32); t128_load(w_gu + (size_t)(r / per) * D * 4096, 4096, r % per, lane, v); }
; }
.LBB0_1344:
	s_waitcnt vmcnt(4)
	v_or_b32_e32 v122, s8, v131
	v_lshlrev_b32_e32 v132, 2, v130
	v_ashrrev_i32_e32 v123, 31, v122
	v_lshl_add_u64 v[124:125], s[16:17], 0, v[132:133]
	v_lshlrev_b64 v[66:67], s14, v[122:123]
	v_lshl_add_u64 v[74:75], v[124:125], 0, v[66:67]
	v_add_u32_e32 v66, 8, v122
	v_ashrrev_i32_e32 v67, 31, v66
	v_lshlrev_b64 v[66:67], s14, v[66:67]
	v_lshl_add_u64 v[76:77], v[124:125], 0, v[66:67]
	global_load_dwordx4 v[70:73], v[74:75], off nt
	global_load_dwordx4 v[66:69], v[76:77], off nt
	v_add_u32_e32 v74, 16, v122
	v_ashrrev_i32_e32 v75, 31, v74
	v_lshlrev_b64 v[74:75], s14, v[74:75]
	v_lshl_add_u64 v[82:83], v[124:125], 0, v[74:75]
	v_add_u32_e32 v74, 24, v122
	v_ashrrev_i32_e32 v75, 31, v74
	v_lshlrev_b64 v[74:75], s14, v[74:75]
	v_lshl_add_u64 v[84:85], v[124:125], 0, v[74:75]
	global_load_dwordx4 v[78:81], v[82:83], off nt
	global_load_dwordx4 v[74:77], v[84:85], off nt
	v_add_u32_e32 v82, 32, v122
	v_ashrrev_i32_e32 v83, 31, v82
	v_lshlrev_b64 v[82:83], s14, v[82:83]
	v_lshl_add_u64 v[90:91], v[124:125], 0, v[82:83]
	v_add_u32_e32 v82, 40, v122
	v_ashrrev_i32_e32 v83, 31, v82
	v_lshlrev_b64 v[82:83], s14, v[82:83]
	v_lshl_add_u64 v[92:93], v[124:125], 0, v[82:83]
	global_load_dwordx4 v[86:89], v[90:91], off nt
	global_load_dwordx4 v[82:85], v[92:93], off nt
	v_add_u32_e32 v90, 48, v122
	v_ashrrev_i32_e32 v91, 31, v90
	v_lshlrev_b64 v[90:91], s14, v[90:91]
	v_lshl_add_u64 v[98:99], v[124:125], 0, v[90:91]
	v_add_u32_e32 v90, 56, v122
	v_ashrrev_i32_e32 v91, 31, v90
	v_lshlrev_b64 v[90:91], s14, v[90:91]
	v_lshl_add_u64 v[100:101], v[124:125], 0, v[90:91]
	global_load_dwordx4 v[94:97], v[98:99], off nt
	global_load_dwordx4 v[90:93], v[100:101], off nt
	v_add_u32_e32 v98, 64, v122
	v_ashrrev_i32_e32 v99, 31, v98
	v_lshlrev_b64 v[98:99], s14, v[98:99]
	v_lshl_add_u64 v[106:107], v[124:125], 0, v[98:99]
	v_add_u32_e32 v98, 0x48, v122
	v_ashrrev_i32_e32 v99, 31, v98
	v_lshlrev_b64 v[98:99], s14, v[98:99]
	v_lshl_add_u64 v[108:109], v[124:125], 0, v[98:99]
	global_load_dwordx4 v[102:105], v[106:107], off nt
	global_load_dwordx4 v[98:101], v[108:109], off nt
	v_add_u32_e32 v106, 0x50, v122
	v_add_u32_e32 v108, 0x58, v122
	v_add_u32_e32 v114, 0x60, v122
	v_add_u32_e32 v116, 0x68, v122
	v_add_u32_e32 v126, 0x70, v122
	v_add_u32_e32 v122, 0x78, v122
	v_ashrrev_i32_e32 v107, 31, v106
	v_ashrrev_i32_e32 v109, 31, v108
	v_ashrrev_i32_e32 v115, 31, v114
	v_ashrrev_i32_e32 v117, 31, v116
	v_ashrrev_i32_e32 v127, 31, v126
	v_ashrrev_i32_e32 v123, 31, v122
	v_lshlrev_b64 v[106:107], s14, v[106:107]
	v_lshlrev_b64 v[108:109], s14, v[108:109]
	v_lshlrev_b64 v[114:115], s14, v[114:115]
	v_lshlrev_b64 v[116:117], s14, v[116:117]
	v_lshlrev_b64 v[126:127], s14, v[126:127]
	v_lshlrev_b64 v[122:123], s14, v[122:123]
	v_lshl_add_u64 v[106:107], v[124:125], 0, v[106:107]
	v_lshl_add_u64 v[108:109], v[124:125], 0, v[108:109]
	v_lshl_add_u64 v[114:115], v[124:125], 0, v[114:115]
	v_lshl_add_u64 v[116:117], v[124:125], 0, v[116:117]
	v_lshl_add_u64 v[126:127], v[124:125], 0, v[126:127]
	v_lshl_add_u64 v[122:123], v[124:125], 0, v[122:123]
	global_load_dwordx4 v[110:113], v[106:107], off nt
	s_nop 0
	global_load_dwordx4 v[106:109], v[108:109], off nt
	s_nop 0
	global_load_dwordx4 v[118:121], v[114:115], off nt
	s_nop 0
	global_load_dwordx4 v[114:117], v[116:117], off nt
	s_nop 0
	global_load_dwordx4 v[126:129], v[126:127], off nt
	s_nop 0
	global_load_dwordx4 v[122:125], v[122:123], off nt
	s_mov_b64 s[14:15], -1
	s_cmpk_gt_i32 s24, 0x7fff
	v_add_u32_e32 v145, 0x1080, v136
	v_add_u32_e32 v146, 0x1088, v136
	v_add_u32_e32 v147, 0x14a0, v136
	v_add_u32_e32 v148, 0x14a8, v136
	v_add_u32_e32 v149, 0x18c0, v136
	v_add_u32_e32 v150, 0x18c8, v136
	v_add_u32_e32 v151, 0x1ce0, v136
	v_add_u32_e32 v152, 0x1ce8, v136
	v_add_u32_e32 v153, 0x2100, v136
	v_add_u32_e32 v154, 0x2108, v136
	v_add_u32_e32 v155, 0x2520, v136
	v_add_u32_e32 v156, 0x2528, v136
	v_add_u32_e32 v157, 0x2940, v136
	v_add_u32_e32 v158, 0x2948, v136
	v_add_u32_e32 v159, 0x2d60, v136
	v_add_u32_e32 v160, 0x2d68, v136
	v_add_u32_e32 v161, 0x3180, v136
	v_add_u32_e32 v162, 0x3188, v136
	v_add_u32_e32 v163, 0x35a0, v136
	v_add_u32_e32 v164, 0x35a8, v136
	v_add_u32_e32 v165, 0x39c0, v136
	v_add_u32_e32 v166, 0x39c8, v136
	v_add_u32_e32 v167, 0x3de0, v136
	v_add_u32_e32 v168, 0x3de8, v136
	v_add_u32_e32 v144, 0x400, v1
	v_add_u32_e32 v143, 0x600, v1
	s_cbranch_scc0 .LBB0_1346
; #define LAS __attribute__((address_space(3)))
; #define LDS_WAIT() asm volatile("s_waitcnt lgkmcnt(0)" ::: "memory")
; template <int MODE>
; __device__ __forceinline__ void t128_store(const Ctx& c, const f32x4 (&v)[16], int K, int N, unsigned char* WT, int item) {
;     LAS float* scr = (LAS float*)(c.lds + c.wave * CONV_SCR);
;     const int nblk = N / 32, kb = item / nblk, nb = item % nblk, k0 = 128 * kb, n0 = 32 * nb, lane = c.lane;
; #pragma unroll
;     for (int i = 0; i < 16; ++i) { LAS float* d = scr + (i * 8 + (lane >> 3)) * 33 + (lane & 7) * 4; d[0] = v[i].x; d[1] = v[i].y; d[2] = v[i].z; d[3] = v[i].w; }
;     LDS_WAIT(); asm volatile("" ::: "memory");
;     const int cc = lane & 7;
; #pragma unroll
;     for (int j = 0; j < 4; ++j) { const int n = (lane >> 3) + 8 * j; const LAS float* s = scr + (16 * cc) * 33 + n; int w[4];
; #pragma unroll
;         for (int q = 0; q < 4; ++q) { int t = 0; t = __builtin_amdgcn_cvt_pk_fp8_f32(s[(4 * q) * 33] * WSCALE, s[(4 * q + 1) * 33] * WSCALE, t, false);
;             t = __builtin_amdgcn_cvt_pk_fp8_f32(s[(4 * q + 2) * 33] * WSCALE, s[(4 * q + 3) * 33] * WSCALE, t, true); w[q] = t; }
	s_waitcnt vmcnt(31)
	ds_write2_b32 v136, v6, v7 offset1:1
	ds_write2_b32 v136, v8, v9 offset0:2 offset1:3
	s_waitcnt vmcnt(30)
	ds_write2_b32 v140, v2, v3 offset1:1
	ds_write2_b32 v140, v4, v5 offset0:2 offset1:3
	s_waitcnt vmcnt(29)
	ds_write2_b32 v141, v14, v15 offset1:1
	ds_write2_b32 v141, v16, v17 offset0:2 offset1:3
	s_waitcnt vmcnt(28)
	ds_write2_b32 v142, v10, v11 offset1:1
	ds_write2_b32 v142, v12, v13 offset0:2 offset1:3
	s_waitcnt vmcnt(27)
	ds_write2_b32 v145, v22, v23 offset1:1
	ds_write2_b32 v146, v24, v25 offset1:1
	s_waitcnt vmcnt(26)
	ds_write2_b32 v147, v18, v19 offset1:1
	ds_write2_b32 v148, v20, v21 offset1:1
	s_waitcnt vmcnt(25)
	ds_write2_b32 v149, v30, v31 offset1:1
	ds_write2_b32 v150, v32, v33 offset1:1
	s_waitcnt vmcnt(24)
	ds_write2_b32 v151, v26, v27 offset1:1
	ds_write2_b32 v152, v28, v29 offset1:1
	s_waitcnt vmcnt(23)
	ds_write2_b32 v153, v38, v39 offset1:1
	ds_write2_b32 v154, v40, v41 offset1:1
	s_waitcnt vmcnt(22)
	ds_write2_b32 v155, v34, v35 offset1:1
	ds_write2_b32 v156, v36, v37 offset1:1
	s_waitcnt vmcnt(21)
	ds_write2_b32 v157, v46, v47 offset1:1
	ds_write2_b32 v158, v48, v49 offset1:1
	s_waitcnt vmcnt(20)
	ds_write2_b32 v159, v42, v43 offset1:1
	ds_write2_b32 v160, v44, v45 offset1:1
	s_waitcnt vmcnt(19)
	ds_write2_b32 v161, v54, v55 offset1:1
	ds_write2_b32 v162, v56, v57 offset1:1
	s_waitcnt vmcnt(18)
	ds_write2_b32 v163, v50, v51 offset1:1
	ds_write2_b32 v164, v52, v53 offset1:1
	s_waitcnt vmcnt(17)
	ds_write2_b32 v165, v62, v63 offset1:1
	ds_write2_b32 v166, v64, v65 offset1:1
	s_waitcnt vmcnt(16)
	ds_write2_b32 v167, v58, v59 offset1:1
	ds_write2_b32 v168, v60, v61 offset1:1
	s_waitcnt lgkmcnt(0)
	ds_read2_b32 v[174:175], v1 offset1:8
	ds_read2_b32 v[176:177], v1 offset0:33 offset1:41
	ds_read2_b32 v[180:181], v1 offset0:66 offset1:74
	ds_read2_b32 v[182:183], v1 offset0:99 offset1:107
	v_mov_b32_e32 v170, v133
	ds_read2_b32 v[184:185], v1 offset0:132 offset1:140
	ds_read2_b32 v[186:187], v1 offset0:165 offset1:173
	s_waitcnt lgkmcnt(5)
	v_mul_f32_e32 v169, 0x42800000, v174
	s_waitcnt lgkmcnt(4)
	v_mul_f32_e32 v171, 0x42800000, v176
	v_cvt_pk_fp8_f32 v170, v169, v171
	s_waitcnt lgkmcnt(3)
	v_mul_f32_e32 v169, 0x42800000, v180
	s_waitcnt lgkmcnt(2)
	v_mul_f32_e32 v171, 0x42800000, v182
	ds_read2_b32 v[188:189], v1 offset0:198 offset1:206
	ds_read2_b32 v[190:191], v1 offset0:231 offset1:239
	v_cvt_pk_fp8_f32 v170, v169, v171 op_sel:[0,0,1]
	s_waitcnt lgkmcnt(3)
	v_mul_f32_e32 v169, 0x42800000, v184
	s_waitcnt lgkmcnt(2)
	v_mul_f32_e32 v172, 0x42800000, v186
	v_mov_b32_e32 v171, v133
	ds_read2_b32 v[192:193], v144 offset0:8 offset1:16
	ds_read2_b32 v[194:195], v144 offset0:41 offset1:49
	v_cvt_pk_fp8_f32 v171, v169, v172
	ds_read2_b32 v[196:197], v144 offset0:74 offset1:82
	ds_read2_b32 v[198:199], v144 offset0:107 offset1:115
	ds_read2_b32 v[200:201], v144 offset0:140 offset1:148
	ds_read2_b32 v[202:203], v144 offset0:173 offset1:181
	s_add_i32 s8, s24, 0xffff8000
	s_lshr_b32 s8, s8, 11
	s_waitcnt lgkmcnt(7)
	v_mul_f32_e32 v169, 0x42800000, v188
	s_waitcnt lgkmcnt(6)
	v_mul_f32_e32 v172, 0x42800000, v190
	s_lshl_b64 s[14:15], s[8:9], 23
	v_cvt_pk_fp8_f32 v171, v169, v172 op_sel:[0,0,1]
	s_waitcnt lgkmcnt(5)
	v_mul_f32_e32 v169, 0x42800000, v192
	s_waitcnt lgkmcnt(4)
	v_mul_f32_e32 v173, 0x42800000, v194
	v_mov_b32_e32 v172, v133
	ds_read2_b32 v[204:205], v144 offset0:206 offset1:214
	ds_read2_b32 v[206:207], v144 offset0:239 offset1:247
	s_add_u32 s8, s52, s14
	v_cvt_pk_fp8_f32 v172, v169, v173
	s_waitcnt lgkmcnt(3)
	v_mul_f32_e32 v176, 0x42800000, v200
	s_waitcnt lgkmcnt(2)
	v_mul_f32_e32 v180, 0x42800000, v202
	v_mov_b32_e32 v173, v133
	s_addc_u32 s15, s53, s15
	s_lshl_b32 s16, s24, 5
	s_and_b32 s14, s24, 0x780
	v_cvt_pk_fp8_f32 v173, v176, v180
	s_add_u32 s14, s8, s14
	s_addc_u32 s15, s15, 0
	v_mul_f32_e32 v169, 0x42800000, v196
	v_mul_f32_e32 v174, 0x42800000, v198
	s_lshl_b32 s8, s24, 6
	v_lshl_add_u64 v[178:179], s[14:15], 0, v[134:135]
	v_cvt_pk_fp8_f32 v172, v169, v174 op_sel:[0,0,1]
	s_waitcnt lgkmcnt(1)
	v_mul_f32_e32 v169, 0x42800000, v204
	s_waitcnt lgkmcnt(0)
; #define LAS __attribute__((address_space(3)))
; #define LDS_WAIT() asm volatile("s_waitcnt lgkmcnt(0)" ::: "memory")
; template <int MODE>
; __device__ __forceinline__ void t128_store(const Ctx& c, const f32x4 (&v)[16], int K, int N, unsigned char* WT, int item) {
;     ...
;     const int cc = lane & 7;
; #pragma unroll
;     for (int j = 0; j < 4; ++j) { const int n = (lane >> 3) + 8 * j; const LAS float* s = scr + (16 * cc) * 33 + n; int w[4];
; #pragma unroll
;         for (int q = 0; q < 4; ++q) { int t = 0; t = __builtin_amdgcn_cvt_pk_fp8_f32(s[(4 * q) * 33] * WSCALE, s[(4 * q + 1) * 33] * WSCALE, t, false);
;             t = __builtin_amdgcn_cvt_pk_fp8_f32(s[(4 * q + 2) * 33] * WSCALE, s[(4 * q + 3) * 33] * WSCALE, t, true); w[q] = t; }
;         const int dr = drow_of<MODE>(n0 + n);
;         __builtin_nontemporal_store((u32x4){(unsigned)w[0], (unsigned)w[1], (unsigned)w[2], (unsigned)w[3]}, (u32x4*)(WT + (size_t)dr * K + k0 + 16 * cc)); }
;     LDS_WAIT(); asm volatile("" ::: "memory");
	v_mul_f32_e32 v174, 0x42800000, v206
	s_and_b32 s8, s8, 0xf00
	s_lshl_b32 s14, s24, 1
	s_and_b32 s15, s16, 0x60
	v_cvt_pk_fp8_f32 v173, v169, v174 op_sel:[0,0,1]
	s_and_b32 s14, s14, 0x80
	s_or_b32 s8, s15, s8
	s_or_b32 s8, s8, s14
	v_add_lshl_u32 v208, s8, v131, 11
	v_mov_b32_e32 v209, v133
	v_lshl_add_u64 v[208:209], v[178:179], 0, v[208:209]
	global_store_dwordx4 v[208:209], v[170:173], off nt
	v_mul_f32_e32 v169, 0x42800000, v175
	v_mul_f32_e32 v174, 0x42800000, v187
	v_mul_f32_e32 v171, 0x42800000, v177
	v_mov_b32_e32 v170, v133
	v_cvt_pk_fp8_f32 v170, v169, v171
	v_mul_f32_e32 v173, 0x42800000, v185
	v_mov_b32_e32 v171, v133
	v_cvt_pk_fp8_f32 v171, v173, v174
	v_mul_f32_e32 v169, 0x42800000, v181
	v_mul_f32_e32 v172, 0x42800000, v183
	v_cvt_pk_fp8_f32 v170, v169, v172 op_sel:[0,0,1]
	v_mul_f32_e32 v169, 0x42800000, v189
	v_mul_f32_e32 v172, 0x42800000, v191
	v_cvt_pk_fp8_f32 v171, v169, v172 op_sel:[0,0,1]
	v_mul_f32_e32 v169, 0x42800000, v193
	v_mul_f32_e32 v173, 0x42800000, v195
	v_mov_b32_e32 v172, v133
	v_cvt_pk_fp8_f32 v172, v169, v173
	v_mul_f32_e32 v175, 0x42800000, v201
	v_mul_f32_e32 v176, 0x42800000, v203
	v_mov_b32_e32 v173, v133
	v_cvt_pk_fp8_f32 v173, v175, v176
	v_mul_f32_e32 v169, 0x42800000, v197
	v_mul_f32_e32 v174, 0x42800000, v199
	v_cvt_pk_fp8_f32 v172, v169, v174 op_sel:[0,0,1]
	v_mul_f32_e32 v169, 0x42800000, v205
	v_mul_f32_e32 v174, 0x42800000, v207
	v_cvt_pk_fp8_f32 v173, v169, v174 op_sel:[0,0,1]
	ds_read2_b32 v[176:177], v1 offset0:16 offset1:24
	ds_read2_b32 v[180:181], v1 offset0:49 offset1:57
	v_add_lshl_u32 v174, s8, v137, 11
	v_mov_b32_e32 v175, v133
	v_lshl_add_u64 v[174:175], v[178:179], 0, v[174:175]
	global_store_dwordx4 v[174:175], v[170:173], off nt
	ds_read2_b32 v[174:175], v1 offset0:82 offset1:90
	ds_read2_b32 v[182:183], v1 offset0:115 offset1:123
	s_waitcnt lgkmcnt(3)
	v_mul_f32_e32 v169, 0x42800000, v176
	s_waitcnt lgkmcnt(2)
	v_mul_f32_e32 v171, 0x42800000, v180
	v_mov_b32_e32 v170, v133
	ds_read2_b32 v[184:185], v1 offset0:148 offset1:156
	ds_read2_b32 v[186:187], v1 offset0:181 offset1:189
	v_cvt_pk_fp8_f32 v170, v169, v171
	s_waitcnt lgkmcnt(3)
	v_mul_f32_e32 v169, 0x42800000, v174
	s_waitcnt lgkmcnt(2)
	v_mul_f32_e32 v171, 0x42800000, v182
	ds_read2_b32 v[188:189], v1 offset0:214 offset1:222
	ds_read2_b32 v[190:191], v1 offset0:247 offset1:255
	v_cvt_pk_fp8_f32 v170, v169, v171 op_sel:[0,0,1]
	s_waitcnt lgkmcnt(3)
	v_mul_f32_e32 v169, 0x42800000, v184
	s_waitcnt lgkmcnt(2)
	v_mul_f32_e32 v172, 0x42800000, v186
	v_mov_b32_e32 v171, v133
	ds_read2_b32 v[192:193], v144 offset0:24 offset1:32
	ds_read2_b32 v[194:195], v144 offset0:57 offset1:65
	v_cvt_pk_fp8_f32 v171, v169, v172
	ds_read2_b32 v[196:197], v144 offset0:90 offset1:98
	ds_read2_b32 v[198:199], v144 offset0:123 offset1:131
	ds_read2_b32 v[200:201], v144 offset0:156 offset1:164
	ds_read2_b32 v[202:203], v144 offset0:189 offset1:197
	s_waitcnt lgkmcnt(7)
	v_mul_f32_e32 v169, 0x42800000, v188
	s_waitcnt lgkmcnt(6)
	v_mul_f32_e32 v172, 0x42800000, v190
	v_cvt_pk_fp8_f32 v171, v169, v172 op_sel:[0,0,1]
	s_waitcnt lgkmcnt(5)
	v_mul_f32_e32 v169, 0x42800000, v192
	s_waitcnt lgkmcnt(4)
	v_mul_f32_e32 v173, 0x42800000, v194
	v_mov_b32_e32 v172, v133
	ds_read2_b32 v[204:205], v144 offset0:222 offset1:230
	ds_read2_b32 v[206:207], v143 offset0:127 offset1:135
	v_cvt_pk_fp8_f32 v172, v169, v173
	s_waitcnt lgkmcnt(3)
	v_mul_f32_e32 v176, 0x42800000, v200
	s_waitcnt lgkmcnt(2)
	v_mul_f32_e32 v180, 0x42800000, v202
	v_mov_b32_e32 v173, v133
	v_cvt_pk_fp8_f32 v173, v176, v180
	v_mul_f32_e32 v169, 0x42800000, v196
	v_mul_f32_e32 v174, 0x42800000, v198
	v_cvt_pk_fp8_f32 v172, v169, v174 op_sel:[0,0,1]
	s_waitcnt lgkmcnt(1)
	v_mul_f32_e32 v169, 0x42800000, v204
	s_waitcnt lgkmcnt(0)
	v_mul_f32_e32 v174, 0x42800000, v206
	v_cvt_pk_fp8_f32 v173, v169, v174 op_sel:[0,0,1]
	v_add_lshl_u32 v208, s8, v138, 11
	v_mov_b32_e32 v209, v133
	v_lshl_add_u64 v[208:209], v[178:179], 0, v[208:209]
	global_store_dwordx4 v[208:209], v[170:173], off nt
	v_mul_f32_e32 v169, 0x42800000, v177
	v_mul_f32_e32 v174, 0x42800000, v187
	v_mul_f32_e32 v171, 0x42800000, v181
	v_mov_b32_e32 v170, v133
	v_cvt_pk_fp8_f32 v170, v169, v171
	v_mul_f32_e32 v173, 0x42800000, v185
	v_mov_b32_e32 v171, v133
	v_cvt_pk_fp8_f32 v171, v173, v174
	v_mul_f32_e32 v169, 0x42800000, v175
	v_mul_f32_e32 v172, 0x42800000, v183
	v_cvt_pk_fp8_f32 v170, v169, v172 op_sel:[0,0,1]
	v_mul_f32_e32 v169, 0x42800000, v189
	v_mul_f32_e32 v172, 0x42800000, v191
	v_cvt_pk_fp8_f32 v171, v169, v172 op_sel:[0,0,1]
	v_mul_f32_e32 v169, 0x42800000, v193
	v_mul_f32_e32 v173, 0x42800000, v195
	v_mov_b32_e32 v172, v133
	v_cvt_pk_fp8_f32 v172, v169, v173
	v_mul_f32_e32 v175, 0x42800000, v201
	v_mul_f32_e32 v176, 0x42800000, v203
	v_mov_b32_e32 v173, v133
	v_cvt_pk_fp8_f32 v173, v175, v176
	v_mul_f32_e32 v169, 0x42800000, v197
	v_mul_f32_e32 v174, 0x42800000, v199
	v_cvt_pk_fp8_f32 v172, v169, v174 op_sel:[0,0,1]
	v_mul_f32_e32 v169, 0x42800000, v205
	v_mul_f32_e32 v174, 0x42800000, v207
	v_cvt_pk_fp8_f32 v173, v169, v174 op_sel:[0,0,1]
	v_add_lshl_u32 v174, s8, v139, 11
	v_mov_b32_e32 v175, v133
	v_lshl_add_u64 v[174:175], v[178:179], 0, v[174:175]
	global_store_dwordx4 v[174:175], v[170:173], off nt
	s_waitcnt lgkmcnt(0)
	s_cbranch_execnz .LBB0_1348
	s_branch .LBB0_1347
